# s12
# speedup vs baseline: 1.0544x; 1.0042x over previous
.LBB1_5:
	v_lshlrev_b32_e32 v67, 4, v1
	v_lshrrev_b32_e32 v1, 1, v1
	v_lshrrev_b32_e32 v69, 5, v132
	v_ashrrev_i32_e32 v66, 4, v132
	v_bitop3_b32 v1, v1, v69, 7 bitop3:0x78
	s_add_u32 s22, s24, s2
	v_lshlrev_b32_e32 v68, 7, v66
	v_lshlrev_b32_e32 v1, 4, v1
	v_and_b32_e32 v0, 8, v0
	s_addc_u32 s90, s25, s3
	v_lshl_or_b32 v201, v66, 12, v67
	v_or3_b32 v0, v68, v1, v0
	v_add_u32_e32 v100, 0x10000, v0
	v_cvt_pk_f16_f32 v1, v64, v65
	v_cvt_pk_f16_f32 v0, v62, v63
	v_cvt_pk_f16_f32 v61, v60, v61
	v_cvt_pk_f16_f32 v60, v58, v59
	ds_write2st64_b64 v100, v[0:1], v[60:61] offset1:8
	v_cvt_pk_f16_f32 v1, v56, v57
	v_cvt_pk_f16_f32 v0, v54, v55
	v_cvt_pk_f16_f32 v53, v52, v53
	v_cvt_pk_f16_f32 v52, v50, v51
	ds_write2st64_b64 v100, v[0:1], v[52:53] offset0:16 offset1:24
	v_cvt_pk_f16_f32 v1, v48, v49
	v_cvt_pk_f16_f32 v0, v46, v47
	v_cvt_pk_f16_f32 v45, v44, v45
	v_cvt_pk_f16_f32 v44, v42, v43
	ds_write2st64_b64 v100, v[0:1], v[44:45] offset0:32 offset1:40
	v_cvt_pk_f16_f32 v1, v40, v41
	v_cvt_pk_f16_f32 v0, v38, v39
	v_cvt_pk_f16_f32 v37, v36, v37
	v_cvt_pk_f16_f32 v36, v34, v35
	ds_write2st64_b64 v100, v[0:1], v[36:37] offset0:48 offset1:56
	s_add_u32 s0, s22, 0x200
	s_addc_u32 s1, s90, 0
	s_add_u32 s70, s0, 0x20000
	s_addc_u32 s71, s1, 0
	s_add_u32 s72, s0, 0x40000
	s_addc_u32 s73, s1, 0
	s_add_u32 s92, s0, 0x60000
	s_addc_u32 s93, s1, 0
	s_add_u32 s94, s0, 0x80000
	s_addc_u32 s95, s1, 0
	s_add_u32 s96, s0, 0xa0000
	s_addc_u32 s97, s1, 0
	s_add_u32 s98, s0, 0xc0000
	s_addc_u32 s99, s1, 0
	s_add_u32 s80, s0, 0xe0000
	s_addc_u32 s81, s1, 0
	global_load_dwordx4 v[70:73], v201, s[0:1] nt
	global_load_dwordx4 v[42:45], v201, s[70:71] nt
	global_load_dwordx4 v[46:49], v201, s[72:73] nt
	global_load_dwordx4 v[66:69], v201, s[92:93] nt
	global_load_dwordx4 v[62:65], v201, s[94:95] nt
	global_load_dwordx4 v[58:61], v201, s[96:97] nt
	global_load_dwordx4 v[54:57], v201, s[98:99] nt
	global_load_dwordx4 v[50:53], v201, s[80:81] nt
	s_waitcnt vmcnt(8)
	s_waitcnt lgkmcnt(0)
	s_barrier
	ds_read_b128 v[34:37], v131
	ds_read_b128 v[38:41], v131 offset:2048
	ds_read_b128 v[74:77], v131 offset:4096
	ds_read_b128 v[78:81], v131 offset:6144
	ds_read_b128 v[82:85], v129
	ds_read_b128 v[86:89], v129 offset:2048
	s_add_u32 s70, s22, 0x300
	v_add_u32_e32 v95, 0x8000, v94
	v_lshl_add_u64 v[0:1], s[26:27], 0, v[196:197]
	s_addc_u32 s71, s90, 0
	v_readfirstlane_b32 s0, v95
	s_mov_b32 m0, s0
	v_cvt_pk_f16_f32 v33, v32, v33
	global_load_lds_dwordx4 v[0:1], off
	v_cvt_pk_f16_f32 v32, v30, v31
	ds_write_b64 v100, v[32:33] offset:32768
	global_load_dwordx4 v[30:33], v201, s[70:71] nt
	s_setprio 1
	s_waitcnt lgkmcnt(1)
	v_mfma_f32_16x16x32_f16 v[90:93], v[82:85], v[34:37], 0
	v_mfma_f32_16x16x32_f16 v[102:105], v[82:85], v[38:41], 0
	v_mfma_f32_16x16x32_f16 v[106:109], v[82:85], v[74:77], 0
	v_mfma_f32_16x16x32_f16 v[82:85], v[82:85], v[78:81], 0
	v_mfma_f32_16x16x32_f16 v[110:113], v[86:89], v[34:37], 0
	v_mfma_f32_16x16x32_f16 v[114:117], v[86:89], v[38:41], 0
	v_mfma_f32_16x16x32_f16 v[118:121], v[86:89], v[74:77], 0
	v_mfma_f32_16x16x32_f16 v[86:89], v[86:89], v[78:81], 0
	s_setprio 0
	ds_read_b128 v[122:125], v129 offset:4096
	ds_read_b128 v[134:137], v129 offset:6144
	v_add_u32_e32 v96, 0xa000, v94
	v_lshl_add_u64 v[98:99], v[0:1], 0, s[58:59]
	v_readfirstlane_b32 s1, v96
	s_mov_b32 m0, s1
	v_cvt_pk_f16_f32 v29, v28, v29
	global_load_lds_dwordx4 v[98:99], off
	v_cvt_pk_f16_f32 v28, v26, v27
	ds_write_b64 v100, v[28:29] offset:36864
	s_add_u32 s70, s22, 0x20300
	s_addc_u32 s71, s90, 0
	global_load_dwordx4 v[26:29], v201, s[70:71] nt
	s_setprio 1
	s_waitcnt lgkmcnt(1)
	v_mfma_f32_16x16x32_f16 v[138:141], v[122:125], v[34:37], 0
	v_mfma_f32_16x16x32_f16 v[142:145], v[122:125], v[38:41], 0
	v_mfma_f32_16x16x32_f16 v[146:149], v[122:125], v[74:77], 0
	v_mfma_f32_16x16x32_f16 v[122:125], v[122:125], v[78:81], 0
	v_mfma_f32_16x16x32_f16 v[150:153], v[134:137], v[34:37], 0
	v_mfma_f32_16x16x32_f16 v[154:157], v[134:137], v[38:41], 0
	v_mfma_f32_16x16x32_f16 v[158:161], v[134:137], v[74:77], 0
	v_mfma_f32_16x16x32_f16 v[134:137], v[134:137], v[78:81], 0
	s_setprio 0
	ds_read_b128 v[162:165], v129 offset:8192
	ds_read_b128 v[166:169], v129 offset:10240
	v_add_u32_e32 v97, 0xc000, v94
	v_lshl_add_u64 v[98:99], v[0:1], 0, s[60:61]
	v_readfirstlane_b32 s71, v97
	s_mov_b32 m0, s71
	v_cvt_pk_f16_f32 v25, v24, v25
	global_load_lds_dwordx4 v[98:99], off
	v_cvt_pk_f16_f32 v24, v22, v23
	ds_write_b64 v100, v[24:25] offset:40960
	s_add_u32 s72, s22, 0x40300
	s_addc_u32 s73, s90, 0
	global_load_dwordx4 v[22:25], v201, s[72:73] nt
	s_setprio 1
	s_waitcnt lgkmcnt(1)
	v_mfma_f32_16x16x32_f16 v[170:173], v[162:165], v[34:37], 0
	v_mfma_f32_16x16x32_f16 v[174:177], v[162:165], v[38:41], 0
	v_mfma_f32_16x16x32_f16 v[178:181], v[162:165], v[74:77], 0
	v_mfma_f32_16x16x32_f16 v[162:165], v[162:165], v[78:81], 0
	v_mfma_f32_16x16x32_f16 v[182:185], v[166:169], v[34:37], 0
	v_mfma_f32_16x16x32_f16 v[186:189], v[166:169], v[38:41], 0
	v_mfma_f32_16x16x32_f16 v[190:193], v[166:169], v[74:77], 0
	v_mfma_f32_16x16x32_f16 v[166:169], v[166:169], v[78:81], 0
	s_setprio 0
	ds_read_b128 v[202:205], v129 offset:12288
	ds_read_b128 v[206:209], v129 offset:14336
	v_add_u32_e32 v98, 0xe000, v94
	v_lshl_add_u64 v[0:1], v[0:1], 0, s[62:63]
	v_readfirstlane_b32 s72, v98
	s_mov_b32 m0, s72
	s_nop 0
	global_load_lds_dwordx4 v[0:1], off
	v_cvt_pk_f16_f32 v1, v20, v21
	v_cvt_pk_f16_f32 v0, v18, v19
	ds_write_b64 v100, v[0:1] offset:45056
	s_add_u32 s80, s22, 0x60300
	s_addc_u32 s81, s90, 0
	global_load_dwordx4 v[18:21], v201, s[80:81] nt
	s_setprio 1
	s_waitcnt lgkmcnt(1)
	v_mfma_f32_16x16x32_f16 v[210:213], v[202:205], v[34:37], 0
	v_mfma_f32_16x16x32_f16 v[214:217], v[202:205], v[38:41], 0
	v_mfma_f32_16x16x32_f16 v[218:221], v[202:205], v[74:77], 0
	v_mfma_f32_16x16x32_f16 v[202:205], v[202:205], v[78:81], 0
	v_mfma_f32_16x16x32_f16 v[74:77], v[206:209], v[74:77], 0
	v_mfma_f32_16x16x32_f16 v[78:81], v[206:209], v[78:81], 0
	v_mfma_f32_16x16x32_f16 v[222:225], v[206:209], v[34:37], 0
	v_mfma_f32_16x16x32_f16 v[226:229], v[206:209], v[38:41], 0
	s_setprio 0
	ds_read_b128 v[206:209], v128
	ds_read_b128 v[230:233], v128 offset:2048
	ds_read_b128 v[234:237], v128 offset:4096
	ds_read_b128 v[238:241], v128 offset:6144
	ds_read_b128 v[34:37], v130
	ds_read_b128 v[38:41], v130 offset:2048
	v_cvt_pk_f16_f32 v1, v16, v17
	v_cvt_pk_f16_f32 v0, v14, v15
	ds_write_b64 v100, v[0:1] offset:49152
	s_add_u32 s80, s22, 0x80300
	s_addc_u32 s81, s90, 0
	global_load_dwordx4 v[14:17], v201, s[80:81] nt
	s_setprio 1
	s_waitcnt lgkmcnt(1)
	v_mfma_f32_16x16x32_f16 v[90:93], v[34:37], v[206:209], v[90:93]
	v_mfma_f32_16x16x32_f16 v[102:105], v[34:37], v[230:233], v[102:105]
	v_mfma_f32_16x16x32_f16 v[106:109], v[34:37], v[234:237], v[106:109]
	v_mfma_f32_16x16x32_f16 v[82:85], v[34:37], v[238:241], v[82:85]
	v_mfma_f32_16x16x32_f16 v[110:113], v[38:41], v[206:209], v[110:113]
	v_mfma_f32_16x16x32_f16 v[114:117], v[38:41], v[230:233], v[114:117]
	v_mfma_f32_16x16x32_f16 v[118:121], v[38:41], v[234:237], v[118:121]
	v_mfma_f32_16x16x32_f16 v[86:89], v[38:41], v[238:241], v[86:89]
	s_setprio 0
	ds_read_b128 v[34:37], v130 offset:4096
	ds_read_b128 v[38:41], v130 offset:6144
	v_cvt_pk_f16_f32 v1, v12, v13
	v_cvt_pk_f16_f32 v0, v10, v11
	ds_write_b64 v100, v[0:1] offset:53248
	s_add_u32 s80, s22, 0xa0300
	s_addc_u32 s81, s90, 0
	global_load_dwordx4 v[10:13], v201, s[80:81] nt
	s_setprio 1
	s_waitcnt lgkmcnt(1)
	v_mfma_f32_16x16x32_f16 v[146:149], v[34:37], v[234:237], v[146:149]
	v_mfma_f32_16x16x32_f16 v[122:125], v[34:37], v[238:241], v[122:125]
	v_mfma_f32_16x16x32_f16 v[134:137], v[38:41], v[238:241], v[134:137]
	v_mfma_f32_16x16x32_f16 v[138:141], v[34:37], v[206:209], v[138:141]
	v_mfma_f32_16x16x32_f16 v[142:145], v[34:37], v[230:233], v[142:145]
	v_mfma_f32_16x16x32_f16 v[150:153], v[38:41], v[206:209], v[150:153]
	v_mfma_f32_16x16x32_f16 v[154:157], v[38:41], v[230:233], v[154:157]
	v_mfma_f32_16x16x32_f16 v[158:161], v[38:41], v[234:237], v[158:161]
	s_setprio 0
	ds_read_b128 v[38:41], v130 offset:8192
	ds_read_b128 v[242:245], v130 offset:10240
	v_cvt_pk_f16_f32 v1, v8, v9
	v_cvt_pk_f16_f32 v0, v6, v7
	ds_write_b64 v100, v[0:1] offset:57344
	s_add_u32 s80, s22, 0xc0300
	s_addc_u32 s81, s90, 0
	global_load_dwordx4 v[34:37], v201, s[80:81] nt
	s_setprio 1
	s_waitcnt lgkmcnt(1)
	v_mfma_f32_16x16x32_f16 v[6:9], v[38:41], v[206:209], v[170:173]
	v_mfma_f32_16x16x32_f16 v[170:173], v[38:41], v[230:233], v[174:177]
	v_mfma_f32_16x16x32_f16 v[174:177], v[38:41], v[234:237], v[178:181]
	v_mfma_f32_16x16x32_f16 v[162:165], v[38:41], v[238:241], v[162:165]
	v_mfma_f32_16x16x32_f16 v[178:181], v[242:245], v[206:209], v[182:185]
	v_mfma_f32_16x16x32_f16 v[182:185], v[242:245], v[230:233], v[186:189]
	v_mfma_f32_16x16x32_f16 v[186:189], v[242:245], v[234:237], v[190:193]
	v_mfma_f32_16x16x32_f16 v[166:169], v[242:245], v[238:241], v[166:169]
	s_setprio 0
	s_nop 0
	ds_read_b128 v[190:193], v130 offset:12288
	ds_read_b128 v[242:245], v130 offset:14336
	v_cvt_pk_f16_f32 v1, v4, v5
	v_cvt_pk_f16_f32 v0, v2, v3
	ds_write_b64 v100, v[0:1] offset:61440
	s_add_u32 s80, s22, 0xe0300
	s_addc_u32 s81, s90, 0
	global_load_dwordx4 v[38:41], v201, s[80:81] nt
	s_setprio 1
	s_waitcnt lgkmcnt(1)
	v_mfma_f32_16x16x32_f16 v[78:81], v[242:245], v[238:241], v[78:81]
	v_mfma_f32_16x16x32_f16 v[210:213], v[190:193], v[206:209], v[210:213]
	v_mfma_f32_16x16x32_f16 v[214:217], v[190:193], v[230:233], v[214:217]
	v_mfma_f32_16x16x32_f16 v[218:221], v[190:193], v[234:237], v[218:221]
	v_mfma_f32_16x16x32_f16 v[190:193], v[190:193], v[238:241], v[202:205]
	v_mfma_f32_16x16x32_f16 v[202:205], v[242:245], v[206:209], v[222:225]
	v_mfma_f32_16x16x32_f16 v[206:209], v[242:245], v[230:233], v[226:229]
	v_mfma_f32_16x16x32_f16 v[222:225], v[242:245], v[234:237], v[74:77]
	s_setprio 0
	s_waitcnt vmcnt(4)
	s_waitcnt lgkmcnt(0)
	s_barrier
	ds_read_b128 v[226:229], v131 offset:32768
	ds_read_b128 v[230:233], v131 offset:34816
	ds_read_b128 v[234:237], v131 offset:36864
	ds_read_b128 v[238:241], v131 offset:38912
	ds_read_b128 v[74:77], v129 offset:32768
	ds_read_b128 v[242:245], v129 offset:34816
	s_add_u32 s80, s22, 0x400
	s_addc_u32 s81, s90, 0
	v_lshl_add_u64 v[198:199], s[28:29], 0, v[196:197]
	v_readfirstlane_b32 s70, v94
	s_mov_b32 m0, s70
	v_cvt_pk_f16_f32 v1, v72, v73
	global_load_lds_dwordx4 v[198:199], off
	v_cvt_pk_f16_f32 v0, v70, v71
	ds_write_b64 v100, v[0:1]
	global_load_dwordx4 v[0:3], v201, s[80:81] nt
	s_setprio 1
	s_waitcnt lgkmcnt(1)
	v_mfma_f32_16x16x32_f16 v[70:73], v[74:77], v[226:229], v[90:93]
	v_mfma_f32_16x16x32_f16 v[90:93], v[74:77], v[230:233], v[102:105]
	v_mfma_f32_16x16x32_f16 v[104:107], v[74:77], v[234:237], v[106:109]
	v_mfma_f32_16x16x32_f16 v[82:85], v[74:77], v[238:241], v[82:85]
	v_mfma_f32_16x16x32_f16 v[108:111], v[242:245], v[226:229], v[110:113]
	v_mfma_f32_16x16x32_f16 v[112:115], v[242:245], v[230:233], v[114:117]
	v_mfma_f32_16x16x32_f16 v[116:119], v[242:245], v[234:237], v[118:121]
	v_mfma_f32_16x16x32_f16 v[86:89], v[242:245], v[238:241], v[86:89]
	s_setprio 0
	ds_read_b128 v[74:77], v129 offset:36864
	ds_read_b128 v[242:245], v129 offset:38912
	v_add_u32_e32 v99, 0x2000, v94
	v_lshl_add_u64 v[4:5], v[198:199], 0, s[58:59]
	v_readfirstlane_b32 s73, v99
	s_mov_b32 m0, s73
	s_nop 0
	global_load_lds_dwordx4 v[4:5], off
	v_cvt_pk_f16_f32 v5, v44, v45
	v_cvt_pk_f16_f32 v4, v42, v43
	ds_write_b64 v100, v[4:5] offset:4096
	s_add_u32 s80, s22, 0x20400
	s_addc_u32 s81, s90, 0
	global_load_dwordx4 v[42:45], v201, s[80:81] nt
	s_setprio 1
	s_waitcnt lgkmcnt(1)
	v_mfma_f32_16x16x32_f16 v[146:149], v[74:77], v[234:237], v[146:149]
	v_mfma_f32_16x16x32_f16 v[120:123], v[74:77], v[238:241], v[122:125]
	v_mfma_f32_16x16x32_f16 v[124:127], v[242:245], v[226:229], v[150:153]
	v_mfma_f32_16x16x32_f16 v[134:137], v[242:245], v[238:241], v[134:137]
	v_mfma_f32_16x16x32_f16 v[138:141], v[74:77], v[226:229], v[138:141]
	v_mfma_f32_16x16x32_f16 v[142:145], v[74:77], v[230:233], v[142:145]
	v_mfma_f32_16x16x32_f16 v[150:153], v[242:245], v[230:233], v[154:157]
	v_mfma_f32_16x16x32_f16 v[154:157], v[242:245], v[234:237], v[158:161]
	s_setprio 0
	ds_read_b128 v[74:77], v129 offset:40960
	s_nop 0
	ds_read_b128 v[158:161], v129 offset:43008
	v_add_u32_e32 v101, 0x4000, v94
	v_lshl_add_u64 v[4:5], v[198:199], 0, s[60:61]
	v_readfirstlane_b32 s91, v101
	s_mov_b32 m0, s91
	s_nop 0
	global_load_lds_dwordx4 v[4:5], off
	v_cvt_pk_f16_f32 v5, v48, v49
	v_cvt_pk_f16_f32 v4, v46, v47
	ds_write_b64 v100, v[4:5] offset:8192
	s_add_u32 s80, s22, 0x40400
	s_addc_u32 s81, s90, 0
	global_load_dwordx4 v[46:49], v201, s[80:81] nt
	s_setprio 1
	s_waitcnt lgkmcnt(1)
	v_mfma_f32_16x16x32_f16 v[4:7], v[74:77], v[226:229], v[6:9]
	v_mfma_f32_16x16x32_f16 v[170:173], v[74:77], v[230:233], v[170:173]
	v_mfma_f32_16x16x32_f16 v[174:177], v[74:77], v[234:237], v[174:177]
	v_mfma_f32_16x16x32_f16 v[162:165], v[74:77], v[238:241], v[162:165]
	v_mfma_f32_16x16x32_f16 v[178:181], v[158:161], v[226:229], v[178:181]
	v_mfma_f32_16x16x32_f16 v[182:185], v[158:161], v[230:233], v[182:185]
	v_mfma_f32_16x16x32_f16 v[186:189], v[158:161], v[234:237], v[186:189]
	v_mfma_f32_16x16x32_f16 v[158:161], v[158:161], v[238:241], v[166:169]
	s_setprio 0
	s_nop 1
	ds_read_b128 v[166:169], v129 offset:45056
	ds_read_b128 v[242:245], v129 offset:47104
	v_add_u32_e32 v102, 0x6000, v94
	v_lshl_add_u64 v[8:9], v[198:199], 0, s[62:63]
	v_readfirstlane_b32 s92, v102
	s_mov_b32 m0, s92
	s_nop 0
	global_load_lds_dwordx4 v[8:9], off
	v_cvt_pk_f16_f32 v9, v68, v69
	v_cvt_pk_f16_f32 v8, v66, v67
	ds_write_b64 v100, v[8:9] offset:12288
	s_add_u32 s80, s22, 0x60400
	s_addc_u32 s81, s90, 0
	global_load_dwordx4 v[74:77], v201, s[80:81] nt
	s_setprio 1
	s_waitcnt lgkmcnt(1)
	v_mfma_f32_16x16x32_f16 v[66:69], v[166:169], v[226:229], v[210:213]
	v_mfma_f32_16x16x32_f16 v[210:213], v[166:169], v[230:233], v[214:217]
	v_mfma_f32_16x16x32_f16 v[214:217], v[166:169], v[234:237], v[218:221]
	v_mfma_f32_16x16x32_f16 v[166:169], v[166:169], v[238:241], v[190:193]
	v_mfma_f32_16x16x32_f16 v[190:193], v[242:245], v[226:229], v[202:205]
	v_mfma_f32_16x16x32_f16 v[202:205], v[242:245], v[230:233], v[206:209]
	v_mfma_f32_16x16x32_f16 v[206:209], v[242:245], v[234:237], v[222:225]
	v_mfma_f32_16x16x32_f16 v[218:221], v[242:245], v[238:241], v[78:81]
	s_setprio 0
	s_nop 0
	ds_read_b128 v[222:225], v128 offset:32768
	ds_read_b128 v[226:229], v128 offset:34816
	ds_read_b128 v[230:233], v128 offset:36864
	ds_read_b128 v[234:237], v128 offset:38912
	ds_read_b128 v[238:241], v130 offset:32768
	ds_read_b128 v[242:245], v130 offset:34816
	v_cvt_pk_f16_f32 v9, v64, v65
	v_cvt_pk_f16_f32 v8, v62, v63
	ds_write_b64 v100, v[8:9] offset:16384
	s_add_u32 s80, s22, 0x80400
	s_addc_u32 s81, s90, 0
	global_load_dwordx4 v[78:81], v201, s[80:81] nt
	s_setprio 1
	s_waitcnt lgkmcnt(1)
	v_mfma_f32_16x16x32_f16 v[62:65], v[238:241], v[222:225], v[70:73]
	v_mfma_f32_16x16x32_f16 v[70:73], v[238:241], v[226:229], v[90:93]
	v_mfma_f32_16x16x32_f16 v[104:107], v[238:241], v[230:233], v[104:107]
	v_mfma_f32_16x16x32_f16 v[108:111], v[242:245], v[222:225], v[108:111]
	v_mfma_f32_16x16x32_f16 v[112:115], v[242:245], v[226:229], v[112:115]
	v_mfma_f32_16x16x32_f16 v[116:119], v[242:245], v[230:233], v[116:119]
	v_mfma_f32_16x16x32_f16 v[238:241], v[238:241], v[234:237], v[82:85]
	v_mfma_f32_16x16x32_f16 v[242:245], v[242:245], v[234:237], v[86:89]
	s_setprio 0
	s_nop 1
	ds_read_b128 v[86:89], v130 offset:36864
	ds_read_b128 v[90:93], v130 offset:38912
	v_cvt_pk_f16_f32 v9, v60, v61
	v_cvt_pk_f16_f32 v8, v58, v59
	ds_write_b64 v100, v[8:9] offset:20480
	s_add_u32 s80, s22, 0xa0400
	s_addc_u32 s81, s90, 0
	global_load_dwordx4 v[82:85], v201, s[80:81] nt
	s_setprio 1
	s_waitcnt lgkmcnt(1)
	v_mfma_f32_16x16x32_f16 v[58:61], v[86:89], v[222:225], v[138:141]
	v_mfma_f32_16x16x32_f16 v[138:141], v[86:89], v[226:229], v[142:145]
	v_mfma_f32_16x16x32_f16 v[142:145], v[86:89], v[230:233], v[146:149]
	v_mfma_f32_16x16x32_f16 v[120:123], v[86:89], v[234:237], v[120:123]
	v_mfma_f32_16x16x32_f16 v[124:127], v[90:93], v[222:225], v[124:127]
	v_mfma_f32_16x16x32_f16 v[146:149], v[90:93], v[226:229], v[150:153]
	v_mfma_f32_16x16x32_f16 v[134:137], v[90:93], v[234:237], v[134:137]
	v_mfma_f32_16x16x32_f16 v[150:153], v[90:93], v[230:233], v[154:157]
	s_setprio 0
	ds_read_b128 v[90:93], v130 offset:40960
	s_nop 0
	ds_read_b128 v[154:157], v130 offset:43008
	v_cvt_pk_f16_f32 v9, v56, v57
	v_cvt_pk_f16_f32 v8, v54, v55
	ds_write_b64 v100, v[8:9] offset:24576
	s_add_u32 s80, s22, 0xc0400
	s_addc_u32 s81, s90, 0
	global_load_dwordx4 v[86:89], v201, s[80:81] nt
	s_setprio 1
	s_waitcnt lgkmcnt(1)
	v_mfma_f32_16x16x32_f16 v[246:249], v[90:93], v[222:225], v[4:7]
	v_mfma_f32_16x16x32_f16 v[170:173], v[90:93], v[226:229], v[170:173]
	v_mfma_f32_16x16x32_f16 v[174:177], v[90:93], v[230:233], v[174:177]
	v_mfma_f32_16x16x32_f16 v[162:165], v[90:93], v[234:237], v[162:165]
	v_mfma_f32_16x16x32_f16 v[178:181], v[154:157], v[222:225], v[178:181]
	v_mfma_f32_16x16x32_f16 v[182:185], v[154:157], v[226:229], v[182:185]
	v_mfma_f32_16x16x32_f16 v[186:189], v[154:157], v[230:233], v[186:189]
	v_mfma_f32_16x16x32_f16 v[154:157], v[154:157], v[234:237], v[158:161]
	s_setprio 0
	ds_read_b128 v[4:7], v130 offset:45056
	ds_read_b128 v[54:57], v130 offset:47104
	v_cvt_pk_f16_f32 v9, v52, v53
	v_cvt_pk_f16_f32 v8, v50, v51
	ds_write_b64 v100, v[8:9] offset:28672
	s_add_u32 s80, s22, 0xe0400
	s_addc_u32 s81, s90, 0
	global_load_dwordx4 v[90:93], v201, s[80:81] nt
	s_setprio 1
	s_waitcnt lgkmcnt(1)
	v_mfma_f32_16x16x32_f16 v[66:69], v[4:7], v[222:225], v[66:69]
	v_mfma_f32_16x16x32_f16 v[158:161], v[4:7], v[226:229], v[210:213]
	v_mfma_f32_16x16x32_f16 v[210:213], v[4:7], v[230:233], v[214:217]
	v_mfma_f32_16x16x32_f16 v[166:169], v[4:7], v[234:237], v[166:169]
	v_mfma_f32_16x16x32_f16 v[190:193], v[54:57], v[222:225], v[190:193]
	v_mfma_f32_16x16x32_f16 v[202:205], v[54:57], v[226:229], v[202:205]
	v_mfma_f32_16x16x32_f16 v[206:209], v[54:57], v[230:233], v[206:209]
	v_mfma_f32_16x16x32_f16 v[214:217], v[54:57], v[234:237], v[218:221]
	s_setprio 0
	s_waitcnt vmcnt(4)
	s_waitcnt lgkmcnt(0)
	s_barrier
	s_nop 0
	ds_read_b128 v[218:221], v131
	ds_read_b128 v[222:225], v131 offset:2048
	ds_read_b128 v[226:229], v131 offset:4096
	ds_read_b128 v[230:233], v131 offset:6144
	ds_read_b128 v[50:53], v129
	ds_read_b128 v[54:57], v129 offset:2048
	s_add_u32 s80, s22, 0x500
	v_lshl_add_u64 v[8:9], s[30:31], 0, v[196:197]
	s_addc_u32 s81, s90, 0
	s_mov_b32 m0, s0
	v_cvt_pk_f16_f32 v5, v32, v33
	global_load_lds_dwordx4 v[8:9], off
	v_cvt_pk_f16_f32 v4, v30, v31
	ds_write_b64 v100, v[4:5] offset:32768
	global_load_dwordx4 v[4:7], v201, s[80:81] nt
	s_setprio 1
	s_waitcnt lgkmcnt(1)
	v_mfma_f32_16x16x32_f16 v[30:33], v[50:53], v[218:221], v[62:65]
	v_mfma_f32_16x16x32_f16 v[70:73], v[50:53], v[222:225], v[70:73]
	v_mfma_f32_16x16x32_f16 v[104:107], v[50:53], v[226:229], v[104:107]
	v_mfma_f32_16x16x32_f16 v[108:111], v[54:57], v[218:221], v[108:111]
	v_mfma_f32_16x16x32_f16 v[112:115], v[54:57], v[222:225], v[112:115]
	v_mfma_f32_16x16x32_f16 v[116:119], v[54:57], v[226:229], v[116:119]
	v_mfma_f32_16x16x32_f16 v[234:237], v[50:53], v[230:233], v[238:241]
	v_mfma_f32_16x16x32_f16 v[238:241], v[54:57], v[230:233], v[242:245]
	s_setprio 0
	ds_read_b128 v[54:57], v129 offset:4096
	ds_read_b128 v[62:65], v129 offset:6144
	s_mov_b32 m0, s1
	v_lshl_add_u64 v[50:51], v[8:9], 0, s[58:59]
	global_load_lds_dwordx4 v[50:51], off
	v_cvt_pk_f16_f32 v29, v28, v29
	v_cvt_pk_f16_f32 v28, v26, v27
	ds_write_b64 v100, v[28:29] offset:36864
	s_add_u32 s0, s22, 0x20500
	s_addc_u32 s1, s90, 0
	global_load_dwordx4 v[50:53], v201, s[0:1] nt
	s_setprio 1
	s_waitcnt lgkmcnt(1)
	v_mfma_f32_16x16x32_f16 v[26:29], v[54:57], v[218:221], v[58:61]
	v_mfma_f32_16x16x32_f16 v[120:123], v[54:57], v[230:233], v[120:123]
	v_mfma_f32_16x16x32_f16 v[124:127], v[62:65], v[218:221], v[124:127]
	v_mfma_f32_16x16x32_f16 v[146:149], v[62:65], v[222:225], v[146:149]
	v_mfma_f32_16x16x32_f16 v[134:137], v[62:65], v[230:233], v[134:137]
	v_mfma_f32_16x16x32_f16 v[138:141], v[54:57], v[222:225], v[138:141]
	v_mfma_f32_16x16x32_f16 v[142:145], v[54:57], v[226:229], v[142:145]
	v_mfma_f32_16x16x32_f16 v[150:153], v[62:65], v[226:229], v[150:153]
	s_setprio 0
	ds_read_b128 v[58:61], v129 offset:8192
	ds_read_b128 v[62:65], v129 offset:10240
	s_mov_b32 m0, s71
	v_lshl_add_u64 v[54:55], v[8:9], 0, s[60:61]
	global_load_lds_dwordx4 v[54:55], off
	v_cvt_pk_f16_f32 v25, v24, v25
	v_cvt_pk_f16_f32 v24, v22, v23
	ds_write_b64 v100, v[24:25] offset:40960
	s_add_u32 s0, s22, 0x40500
	s_addc_u32 s1, s90, 0
	global_load_dwordx4 v[54:57], v201, s[0:1] nt
	s_setprio 1
	s_waitcnt lgkmcnt(1)
	v_mfma_f32_16x16x32_f16 v[22:25], v[58:61], v[218:221], v[246:249]
	v_mfma_f32_16x16x32_f16 v[170:173], v[58:61], v[222:225], v[170:173]
	v_mfma_f32_16x16x32_f16 v[174:177], v[58:61], v[226:229], v[174:177]
	v_mfma_f32_16x16x32_f16 v[162:165], v[58:61], v[230:233], v[162:165]
	v_mfma_f32_16x16x32_f16 v[178:181], v[62:65], v[218:221], v[178:181]
	v_mfma_f32_16x16x32_f16 v[182:185], v[62:65], v[222:225], v[182:185]
	v_mfma_f32_16x16x32_f16 v[186:189], v[62:65], v[226:229], v[186:189]
	v_mfma_f32_16x16x32_f16 v[154:157], v[62:65], v[230:233], v[154:157]
	s_setprio 0
	ds_read_b128 v[62:65], v129 offset:12288
	ds_read_b128 v[242:245], v129 offset:14336
	s_mov_b32 m0, s72
	v_lshl_add_u64 v[8:9], v[8:9], 0, s[62:63]
	global_load_lds_dwordx4 v[8:9], off
	v_cvt_pk_f16_f32 v9, v20, v21
	v_cvt_pk_f16_f32 v8, v18, v19
	ds_write_b64 v100, v[8:9] offset:45056
	s_add_u32 s0, s22, 0x60500
	s_addc_u32 s1, s90, 0
	global_load_dwordx4 v[58:61], v201, s[0:1] nt
	s_setprio 1
	s_waitcnt lgkmcnt(1)
	v_mfma_f32_16x16x32_f16 v[18:21], v[62:65], v[218:221], v[66:69]
	v_mfma_f32_16x16x32_f16 v[158:161], v[62:65], v[222:225], v[158:161]
	v_mfma_f32_16x16x32_f16 v[210:213], v[62:65], v[226:229], v[210:213]
	v_mfma_f32_16x16x32_f16 v[166:169], v[62:65], v[230:233], v[166:169]
	v_mfma_f32_16x16x32_f16 v[190:193], v[242:245], v[218:221], v[190:193]
	v_mfma_f32_16x16x32_f16 v[202:205], v[242:245], v[222:225], v[202:205]
	v_mfma_f32_16x16x32_f16 v[206:209], v[242:245], v[226:229], v[206:209]
	v_mfma_f32_16x16x32_f16 v[214:217], v[242:245], v[230:233], v[214:217]
	s_setprio 0
	ds_read_b128 v[218:221], v128
	ds_read_b128 v[222:225], v128 offset:2048
	ds_read_b128 v[226:229], v128 offset:4096
	ds_read_b128 v[230:233], v128 offset:6144
	ds_read_b128 v[66:69], v130
	ds_read_b128 v[242:245], v130 offset:2048
	v_cvt_pk_f16_f32 v9, v16, v17
	v_cvt_pk_f16_f32 v8, v14, v15
	ds_write_b64 v100, v[8:9] offset:49152
	s_add_u32 s0, s22, 0x80500
	s_addc_u32 s1, s90, 0
	global_load_dwordx4 v[62:65], v201, s[0:1] nt
	s_setprio 1
	s_waitcnt lgkmcnt(1)
	v_mfma_f32_16x16x32_f16 v[14:17], v[66:69], v[218:221], v[30:33]
	v_mfma_f32_16x16x32_f16 v[30:33], v[66:69], v[222:225], v[70:73]
	v_mfma_f32_16x16x32_f16 v[104:107], v[66:69], v[226:229], v[104:107]
	v_mfma_f32_16x16x32_f16 v[108:111], v[242:245], v[218:221], v[108:111]
	v_mfma_f32_16x16x32_f16 v[112:115], v[242:245], v[222:225], v[112:115]
	v_mfma_f32_16x16x32_f16 v[116:119], v[242:245], v[226:229], v[116:119]
	v_mfma_f32_16x16x32_f16 v[234:237], v[66:69], v[230:233], v[234:237]
	v_mfma_f32_16x16x32_f16 v[238:241], v[242:245], v[230:233], v[238:241]
	s_setprio 0
	ds_read_b128 v[70:73], v130 offset:4096
	ds_read_b128 v[242:245], v130 offset:6144
	v_cvt_pk_f16_f32 v9, v12, v13
	v_cvt_pk_f16_f32 v8, v10, v11
	ds_write_b64 v100, v[8:9] offset:53248
	s_add_u32 s0, s22, 0xa0500
	s_addc_u32 s1, s90, 0
	global_load_dwordx4 v[66:69], v201, s[0:1] nt
	s_setprio 1
	s_waitcnt lgkmcnt(1)
	v_mfma_f32_16x16x32_f16 v[26:29], v[70:73], v[218:221], v[26:29]
	v_mfma_f32_16x16x32_f16 v[120:123], v[70:73], v[230:233], v[120:123]
	v_mfma_f32_16x16x32_f16 v[124:127], v[242:245], v[218:221], v[124:127]
	v_mfma_f32_16x16x32_f16 v[146:149], v[242:245], v[222:225], v[146:149]
	v_mfma_f32_16x16x32_f16 v[134:137], v[242:245], v[230:233], v[134:137]
	v_mfma_f32_16x16x32_f16 v[138:141], v[70:73], v[222:225], v[138:141]
	v_mfma_f32_16x16x32_f16 v[142:145], v[70:73], v[226:229], v[142:145]
	v_mfma_f32_16x16x32_f16 v[150:153], v[242:245], v[226:229], v[150:153]
	s_setprio 0
	ds_read_b128 v[8:11], v130 offset:8192
	ds_read_b128 v[242:245], v130 offset:10240
	v_cvt_pk_f16_f32 v13, v36, v37
	v_cvt_pk_f16_f32 v12, v34, v35
	ds_write_b64 v100, v[12:13] offset:57344
	s_add_u32 s0, s22, 0xc0500
	s_addc_u32 s1, s90, 0
	global_load_dwordx4 v[70:73], v201, s[0:1] nt
	s_setprio 1
	s_waitcnt lgkmcnt(1)
	v_mfma_f32_16x16x32_f16 v[22:25], v[8:11], v[218:221], v[22:25]
	v_mfma_f32_16x16x32_f16 v[170:173], v[8:11], v[222:225], v[170:173]
	v_mfma_f32_16x16x32_f16 v[174:177], v[8:11], v[226:229], v[174:177]
	v_mfma_f32_16x16x32_f16 v[162:165], v[8:11], v[230:233], v[162:165]
	v_mfma_f32_16x16x32_f16 v[178:181], v[242:245], v[218:221], v[178:181]
	v_mfma_f32_16x16x32_f16 v[182:185], v[242:245], v[222:225], v[182:185]
	v_mfma_f32_16x16x32_f16 v[186:189], v[242:245], v[226:229], v[186:189]
	v_mfma_f32_16x16x32_f16 v[154:157], v[242:245], v[230:233], v[154:157]
	s_setprio 0
	ds_read_b128 v[8:11], v130 offset:12288
	ds_read_b128 v[242:245], v130 offset:14336
	v_cvt_pk_f16_f32 v13, v40, v41
	v_cvt_pk_f16_f32 v12, v38, v39
	ds_write_b64 v100, v[12:13] offset:61440
	s_add_u32 s0, s22, 0xe0500
	s_addc_u32 s1, s90, 0
	global_load_dwordx4 v[36:39], v201, s[0:1] nt
	s_setprio 1
	s_waitcnt lgkmcnt(1)
	v_mfma_f32_16x16x32_f16 v[246:249], v[8:11], v[218:221], v[18:21]
	v_mfma_f32_16x16x32_f16 v[158:161], v[8:11], v[222:225], v[158:161]
	v_mfma_f32_16x16x32_f16 v[210:213], v[8:11], v[226:229], v[210:213]
	v_mfma_f32_16x16x32_f16 v[166:169], v[8:11], v[230:233], v[166:169]
	v_mfma_f32_16x16x32_f16 v[190:193], v[242:245], v[218:221], v[190:193]
	v_mfma_f32_16x16x32_f16 v[202:205], v[242:245], v[222:225], v[202:205]
	v_mfma_f32_16x16x32_f16 v[206:209], v[242:245], v[226:229], v[206:209]
	v_mfma_f32_16x16x32_f16 v[214:217], v[242:245], v[230:233], v[214:217]
	s_setprio 0
	s_waitcnt vmcnt(4)
	s_waitcnt lgkmcnt(0)
	s_barrier
	ds_read_b128 v[218:221], v131 offset:32768
	ds_read_b128 v[222:225], v131 offset:34816
	ds_read_b128 v[226:229], v131 offset:36864
	ds_read_b128 v[230:233], v131 offset:38912
	ds_read_b128 v[8:11], v129 offset:32768
	ds_read_b128 v[18:21], v129 offset:34816
	s_add_u32 s0, s22, 0x600
	s_addc_u32 s1, s90, 0
	v_lshl_add_u64 v[34:35], s[34:35], 0, v[196:197]
	s_mov_b32 m0, s70
	v_cvt_pk_f16_f32 v3, v2, v3
	global_load_lds_dwordx4 v[34:35], off
	v_cvt_pk_f16_f32 v2, v0, v1
	ds_write_b64 v100, v[2:3]
	global_load_dwordx4 v[0:3], v201, s[0:1] nt
	s_setprio 1
	s_waitcnt lgkmcnt(1)
	v_mfma_f32_16x16x32_f16 v[30:33], v[8:11], v[222:225], v[30:33]
	v_mfma_f32_16x16x32_f16 v[104:107], v[8:11], v[226:229], v[104:107]
	v_mfma_f32_16x16x32_f16 v[108:111], v[18:21], v[218:221], v[108:111]
	v_mfma_f32_16x16x32_f16 v[112:115], v[18:21], v[222:225], v[112:115]
	v_mfma_f32_16x16x32_f16 v[116:119], v[18:21], v[226:229], v[116:119]
	v_mfma_f32_16x16x32_f16 v[242:245], v[8:11], v[218:221], v[14:17]
	v_mfma_f32_16x16x32_f16 v[234:237], v[8:11], v[230:233], v[234:237]
	v_mfma_f32_16x16x32_f16 v[238:241], v[18:21], v[230:233], v[238:241]
	s_setprio 0
	ds_read_b128 v[12:15], v129 offset:36864
	ds_read_b128 v[16:19], v129 offset:38912
	s_mov_b32 m0, s73
	v_lshl_add_u64 v[8:9], v[34:35], 0, s[58:59]
	global_load_lds_dwordx4 v[8:9], off
	v_cvt_pk_f16_f32 v9, v44, v45
	v_cvt_pk_f16_f32 v8, v42, v43
	ds_write_b64 v100, v[8:9] offset:4096
	s_add_u32 s0, s22, 0x20600
	s_addc_u32 s1, s90, 0
	global_load_dwordx4 v[8:11], v201, s[0:1] nt
	s_setprio 1
	s_waitcnt lgkmcnt(1)
	v_mfma_f32_16x16x32_f16 v[40:43], v[12:15], v[218:221], v[26:29]
	v_mfma_f32_16x16x32_f16 v[120:123], v[12:15], v[230:233], v[120:123]
	v_mfma_f32_16x16x32_f16 v[124:127], v[16:19], v[218:221], v[124:127]
	v_mfma_f32_16x16x32_f16 v[146:149], v[16:19], v[222:225], v[146:149]
	v_mfma_f32_16x16x32_f16 v[134:137], v[16:19], v[230:233], v[134:137]
	v_mfma_f32_16x16x32_f16 v[138:141], v[12:15], v[222:225], v[138:141]
	v_mfma_f32_16x16x32_f16 v[142:145], v[12:15], v[226:229], v[142:145]
	v_mfma_f32_16x16x32_f16 v[150:153], v[16:19], v[226:229], v[150:153]
	s_setprio 0
	ds_read_b128 v[16:19], v129 offset:40960
	ds_read_b128 v[26:29], v129 offset:43008
	s_mov_b32 m0, s91
	v_lshl_add_u64 v[12:13], v[34:35], 0, s[60:61]
	global_load_lds_dwordx4 v[12:13], off
	v_cvt_pk_f16_f32 v13, v48, v49
	v_cvt_pk_f16_f32 v12, v46, v47
	ds_write_b64 v100, v[12:13] offset:8192
	s_add_u32 s0, s22, 0x40600
	s_addc_u32 s1, s90, 0
	global_load_dwordx4 v[12:15], v201, s[0:1] nt
	s_setprio 1
	s_waitcnt lgkmcnt(1)
	v_mfma_f32_16x16x32_f16 v[44:47], v[16:19], v[218:221], v[22:25]
	v_mfma_f32_16x16x32_f16 v[170:173], v[16:19], v[222:225], v[170:173]
	v_mfma_f32_16x16x32_f16 v[174:177], v[16:19], v[226:229], v[174:177]
	v_mfma_f32_16x16x32_f16 v[162:165], v[16:19], v[230:233], v[162:165]
	v_mfma_f32_16x16x32_f16 v[178:181], v[26:29], v[218:221], v[178:181]
	v_mfma_f32_16x16x32_f16 v[182:185], v[26:29], v[222:225], v[182:185]
	v_mfma_f32_16x16x32_f16 v[186:189], v[26:29], v[226:229], v[186:189]
	v_mfma_f32_16x16x32_f16 v[154:157], v[26:29], v[230:233], v[154:157]
	s_setprio 0
	ds_read_b128 v[20:23], v129 offset:45056
	ds_read_b128 v[24:27], v129 offset:47104
	s_mov_b32 m0, s92
	v_lshl_add_u64 v[16:17], v[34:35], 0, s[62:63]
	global_load_lds_dwordx4 v[16:17], off
	v_cvt_pk_f16_f32 v17, v76, v77
	v_cvt_pk_f16_f32 v16, v74, v75
	ds_write_b64 v100, v[16:17] offset:12288
	s_add_u32 s0, s22, 0x60600
	s_addc_u32 s1, s90, 0
	global_load_dwordx4 v[16:19], v201, s[0:1] nt
	s_setprio 1
	s_waitcnt lgkmcnt(1)
	v_mfma_f32_16x16x32_f16 v[74:77], v[20:23], v[218:221], v[246:249]
	v_mfma_f32_16x16x32_f16 v[158:161], v[20:23], v[222:225], v[158:161]
	v_mfma_f32_16x16x32_f16 v[210:213], v[20:23], v[226:229], v[210:213]
	v_mfma_f32_16x16x32_f16 v[166:169], v[20:23], v[230:233], v[166:169]
	v_mfma_f32_16x16x32_f16 v[190:193], v[24:27], v[218:221], v[190:193]
	v_mfma_f32_16x16x32_f16 v[202:205], v[24:27], v[222:225], v[202:205]
	v_mfma_f32_16x16x32_f16 v[206:209], v[24:27], v[226:229], v[206:209]
	v_mfma_f32_16x16x32_f16 v[214:217], v[24:27], v[230:233], v[214:217]
	s_setprio 0
	ds_read_b128 v[218:221], v128 offset:32768
	ds_read_b128 v[222:225], v128 offset:34816
	ds_read_b128 v[226:229], v128 offset:36864
	ds_read_b128 v[230:233], v128 offset:38912
	ds_read_b128 v[24:27], v130 offset:32768
	ds_read_b128 v[246:249], v130 offset:34816
	v_cvt_pk_f16_f32 v21, v80, v81
	v_cvt_pk_f16_f32 v20, v78, v79
	ds_write_b64 v100, v[20:21] offset:16384
	s_add_u32 s0, s22, 0x80600
	s_addc_u32 s1, s90, 0
	global_load_dwordx4 v[20:23], v201, s[0:1] nt
	s_setprio 1
	s_waitcnt lgkmcnt(1)
	v_mfma_f32_16x16x32_f16 v[78:81], v[24:27], v[218:221], v[242:245]
	v_mfma_f32_16x16x32_f16 v[104:107], v[24:27], v[226:229], v[104:107]
	v_mfma_f32_16x16x32_f16 v[108:111], v[246:249], v[218:221], v[108:111]
	v_mfma_f32_16x16x32_f16 v[112:115], v[246:249], v[222:225], v[112:115]
	v_mfma_f32_16x16x32_f16 v[116:119], v[246:249], v[226:229], v[116:119]
	v_mfma_f32_16x16x32_f16 v[242:245], v[24:27], v[222:225], v[30:33]
	v_mfma_f32_16x16x32_f16 v[234:237], v[24:27], v[230:233], v[234:237]
	v_mfma_f32_16x16x32_f16 v[238:241], v[246:249], v[230:233], v[238:241]
	s_setprio 0
	ds_read_b128 v[28:31], v130 offset:36864
	ds_read_b128 v[32:35], v130 offset:38912
	v_cvt_pk_f16_f32 v25, v84, v85
	v_cvt_pk_f16_f32 v24, v82, v83
	ds_write_b64 v100, v[24:25] offset:20480
	s_add_u32 s0, s22, 0xa0600
	s_addc_u32 s1, s90, 0
	global_load_dwordx4 v[24:27], v201, s[0:1] nt
	s_setprio 1
	s_waitcnt lgkmcnt(1)
	v_mfma_f32_16x16x32_f16 v[82:85], v[28:31], v[218:221], v[40:43]
	v_mfma_f32_16x16x32_f16 v[120:123], v[28:31], v[230:233], v[120:123]
	v_mfma_f32_16x16x32_f16 v[124:127], v[32:35], v[218:221], v[124:127]
	v_mfma_f32_16x16x32_f16 v[146:149], v[32:35], v[222:225], v[146:149]
	v_mfma_f32_16x16x32_f16 v[134:137], v[32:35], v[230:233], v[134:137]
	v_mfma_f32_16x16x32_f16 v[138:141], v[28:31], v[222:225], v[138:141]
	v_mfma_f32_16x16x32_f16 v[142:145], v[28:31], v[226:229], v[142:145]
	v_mfma_f32_16x16x32_f16 v[150:153], v[32:35], v[226:229], v[150:153]
	s_setprio 0
	ds_read_b128 v[32:35], v130 offset:40960
	ds_read_b128 v[40:43], v130 offset:43008
	v_cvt_pk_f16_f32 v29, v88, v89
	v_cvt_pk_f16_f32 v28, v86, v87
	ds_write_b64 v100, v[28:29] offset:24576
	s_add_u32 s0, s22, 0xc0600
	s_addc_u32 s1, s90, 0
	global_load_dwordx4 v[28:31], v201, s[0:1] nt
	s_setprio 1
	s_waitcnt lgkmcnt(1)
	v_mfma_f32_16x16x32_f16 v[86:89], v[32:35], v[218:221], v[44:47]
	v_mfma_f32_16x16x32_f16 v[170:173], v[32:35], v[222:225], v[170:173]
	v_mfma_f32_16x16x32_f16 v[174:177], v[32:35], v[226:229], v[174:177]
	v_mfma_f32_16x16x32_f16 v[162:165], v[32:35], v[230:233], v[162:165]
	v_mfma_f32_16x16x32_f16 v[178:181], v[40:43], v[218:221], v[178:181]
	v_mfma_f32_16x16x32_f16 v[182:185], v[40:43], v[222:225], v[182:185]
	v_mfma_f32_16x16x32_f16 v[186:189], v[40:43], v[226:229], v[186:189]
	v_mfma_f32_16x16x32_f16 v[154:157], v[40:43], v[230:233], v[154:157]
	s_setprio 0
	ds_read_b128 v[40:43], v130 offset:45056
	ds_read_b128 v[44:47], v130 offset:47104
	v_cvt_pk_f16_f32 v33, v92, v93
	v_cvt_pk_f16_f32 v32, v90, v91
	ds_write_b64 v100, v[32:33] offset:28672
	s_add_u32 s0, s22, 0xe0600
	s_addc_u32 s1, s90, 0
	global_load_dwordx4 v[32:35], v201, s[0:1] nt
	s_setprio 1
	s_waitcnt lgkmcnt(1)
	v_mfma_f32_16x16x32_f16 v[74:77], v[40:43], v[218:221], v[74:77]
	v_mfma_f32_16x16x32_f16 v[90:93], v[40:43], v[222:225], v[158:161]
	v_mfma_f32_16x16x32_f16 v[158:161], v[40:43], v[226:229], v[210:213]
	v_mfma_f32_16x16x32_f16 v[166:169], v[40:43], v[230:233], v[166:169]
	v_mfma_f32_16x16x32_f16 v[190:193], v[44:47], v[218:221], v[190:193]
	v_mfma_f32_16x16x32_f16 v[202:205], v[44:47], v[222:225], v[202:205]
	v_mfma_f32_16x16x32_f16 v[206:209], v[44:47], v[226:229], v[206:209]
	v_mfma_f32_16x16x32_f16 v[210:213], v[44:47], v[230:233], v[214:217]
	s_setprio 0
	s_waitcnt vmcnt(4)
	s_waitcnt lgkmcnt(0)
	s_barrier
	s_nop 0
	ds_read_b128 v[214:217], v131
	ds_read_b128 v[218:221], v131 offset:2048
	ds_read_b128 v[222:225], v131 offset:4096
	ds_read_b128 v[226:229], v131 offset:6144
	ds_read_b128 v[40:43], v129
	ds_read_b128 v[44:47], v129 offset:2048
	s_add_u32 s70, s22, 0x700
	s_addc_u32 s71, s90, 0
	v_lshl_add_u64 v[198:199], s[36:37], 0, v[196:197]
	v_readfirstlane_b32 s0, v95
	s_mov_b32 m0, s0
	v_cvt_pk_f16_f32 v7, v6, v7
	global_load_lds_dwordx4 v[198:199], off
	v_cvt_pk_f16_f32 v6, v4, v5
	ds_write_b64 v100, v[6:7] offset:32768
	global_load_dwordx4 v[4:7], v201, s[70:71] nt
	s_setprio 1
	s_waitcnt lgkmcnt(1)
	v_mfma_f32_16x16x32_f16 v[78:81], v[40:43], v[214:217], v[78:81]
	v_mfma_f32_16x16x32_f16 v[104:107], v[40:43], v[222:225], v[104:107]
	v_mfma_f32_16x16x32_f16 v[108:111], v[44:47], v[214:217], v[108:111]
	v_mfma_f32_16x16x32_f16 v[112:115], v[44:47], v[218:221], v[112:115]
	v_mfma_f32_16x16x32_f16 v[116:119], v[44:47], v[222:225], v[116:119]
	v_mfma_f32_16x16x32_f16 v[230:233], v[40:43], v[218:221], v[242:245]
	v_mfma_f32_16x16x32_f16 v[234:237], v[40:43], v[226:229], v[234:237]
	v_mfma_f32_16x16x32_f16 v[238:241], v[44:47], v[226:229], v[238:241]
	s_setprio 0
	ds_read_b128 v[44:47], v129 offset:4096
	ds_read_b128 v[242:245], v129 offset:6144
	v_readfirstlane_b32 s72, v96
	v_lshl_add_u64 v[40:41], v[198:199], 0, s[58:59]
	s_mov_b32 m0, s72
	s_nop 0
	global_load_lds_dwordx4 v[40:41], off
	v_cvt_pk_f16_f32 v41, v52, v53
	v_cvt_pk_f16_f32 v40, v50, v51
	ds_write_b64 v100, v[40:41] offset:36864
	s_add_u32 s70, s22, 0x20700
	s_addc_u32 s71, s90, 0
	global_load_dwordx4 v[40:43], v201, s[70:71] nt
	s_setprio 1
	s_waitcnt lgkmcnt(1)
	v_mfma_f32_16x16x32_f16 v[82:85], v[44:47], v[214:217], v[82:85]
	v_mfma_f32_16x16x32_f16 v[120:123], v[44:47], v[226:229], v[120:123]
	v_mfma_f32_16x16x32_f16 v[124:127], v[242:245], v[214:217], v[124:127]
	v_mfma_f32_16x16x32_f16 v[146:149], v[242:245], v[218:221], v[146:149]
	v_mfma_f32_16x16x32_f16 v[134:137], v[242:245], v[226:229], v[134:137]
	v_mfma_f32_16x16x32_f16 v[138:141], v[44:47], v[218:221], v[138:141]
	v_mfma_f32_16x16x32_f16 v[142:145], v[44:47], v[222:225], v[142:145]
	v_mfma_f32_16x16x32_f16 v[150:153], v[242:245], v[222:225], v[150:153]
	s_setprio 0
	ds_read_b128 v[48:51], v129 offset:8192
	ds_read_b128 v[242:245], v129 offset:10240
	v_readfirstlane_b32 s71, v97
	v_lshl_add_u64 v[44:45], v[198:199], 0, s[60:61]
	s_mov_b32 m0, s71
	s_nop 0
	global_load_lds_dwordx4 v[44:45], off
	v_cvt_pk_f16_f32 v45, v56, v57
	v_cvt_pk_f16_f32 v44, v54, v55
	ds_write_b64 v100, v[44:45] offset:40960
	s_add_u32 s80, s22, 0x40700
	s_addc_u32 s81, s90, 0
	global_load_dwordx4 v[44:47], v201, s[80:81] nt
	s_setprio 1
	s_waitcnt lgkmcnt(1)
	v_mfma_f32_16x16x32_f16 v[86:89], v[48:51], v[214:217], v[86:89]
	v_mfma_f32_16x16x32_f16 v[170:173], v[48:51], v[218:221], v[170:173]
	v_mfma_f32_16x16x32_f16 v[174:177], v[48:51], v[222:225], v[174:177]
	v_mfma_f32_16x16x32_f16 v[162:165], v[48:51], v[226:229], v[162:165]
	v_mfma_f32_16x16x32_f16 v[178:181], v[242:245], v[214:217], v[178:181]
	v_mfma_f32_16x16x32_f16 v[182:185], v[242:245], v[218:221], v[182:185]
	v_mfma_f32_16x16x32_f16 v[186:189], v[242:245], v[222:225], v[186:189]
	v_mfma_f32_16x16x32_f16 v[154:157], v[242:245], v[226:229], v[154:157]
	s_setprio 0
	ds_read_b128 v[52:55], v129 offset:12288
	ds_read_b128 v[242:245], v129 offset:14336
	v_readfirstlane_b32 s70, v98
	v_lshl_add_u64 v[48:49], v[198:199], 0, s[62:63]
	s_mov_b32 m0, s70
	s_nop 0
	global_load_lds_dwordx4 v[48:49], off
	v_cvt_pk_f16_f32 v49, v60, v61
	v_cvt_pk_f16_f32 v48, v58, v59
	ds_write_b64 v100, v[48:49] offset:45056
	s_add_u32 s80, s22, 0x60700
	s_addc_u32 s81, s90, 0
	global_load_dwordx4 v[48:51], v201, s[80:81] nt
	s_setprio 1
	s_waitcnt lgkmcnt(1)
	v_mfma_f32_16x16x32_f16 v[74:77], v[52:55], v[214:217], v[74:77]
	v_mfma_f32_16x16x32_f16 v[90:93], v[52:55], v[218:221], v[90:93]
	v_mfma_f32_16x16x32_f16 v[158:161], v[52:55], v[222:225], v[158:161]
	v_mfma_f32_16x16x32_f16 v[166:169], v[52:55], v[226:229], v[166:169]
	v_mfma_f32_16x16x32_f16 v[190:193], v[242:245], v[214:217], v[190:193]
	v_mfma_f32_16x16x32_f16 v[202:205], v[242:245], v[218:221], v[202:205]
	v_mfma_f32_16x16x32_f16 v[206:209], v[242:245], v[222:225], v[206:209]
	v_mfma_f32_16x16x32_f16 v[210:213], v[242:245], v[226:229], v[210:213]
	s_setprio 0
	ds_read_b128 v[214:217], v128
	ds_read_b128 v[218:221], v128 offset:2048
	ds_read_b128 v[222:225], v128 offset:4096
	ds_read_b128 v[226:229], v128 offset:6144
	ds_read_b128 v[56:59], v130
	ds_read_b128 v[242:245], v130 offset:2048
	v_cvt_pk_f16_f32 v53, v64, v65
	v_cvt_pk_f16_f32 v52, v62, v63
	ds_write_b64 v100, v[52:53] offset:49152
	s_add_u32 s80, s22, 0x80700
	s_addc_u32 s81, s90, 0
	global_load_dwordx4 v[52:55], v201, s[80:81] nt
	s_setprio 1
	s_waitcnt lgkmcnt(1)
	v_mfma_f32_16x16x32_f16 v[78:81], v[56:59], v[214:217], v[78:81]
	v_mfma_f32_16x16x32_f16 v[104:107], v[56:59], v[222:225], v[104:107]
	v_mfma_f32_16x16x32_f16 v[108:111], v[242:245], v[214:217], v[108:111]
	v_mfma_f32_16x16x32_f16 v[112:115], v[242:245], v[218:221], v[112:115]
	v_mfma_f32_16x16x32_f16 v[116:119], v[242:245], v[222:225], v[116:119]
	v_mfma_f32_16x16x32_f16 v[230:233], v[56:59], v[218:221], v[230:233]
	v_mfma_f32_16x16x32_f16 v[234:237], v[56:59], v[226:229], v[234:237]
	v_mfma_f32_16x16x32_f16 v[238:241], v[242:245], v[226:229], v[238:241]
	s_setprio 0
	ds_read_b128 v[60:63], v130 offset:4096
	ds_read_b128 v[242:245], v130 offset:6144
	v_cvt_pk_f16_f32 v57, v68, v69
	v_cvt_pk_f16_f32 v56, v66, v67
	ds_write_b64 v100, v[56:57] offset:53248
	s_add_u32 s80, s22, 0xa0700
	s_addc_u32 s81, s90, 0
	global_load_dwordx4 v[56:59], v201, s[80:81] nt
	s_setprio 1
	s_waitcnt lgkmcnt(1)
	v_mfma_f32_16x16x32_f16 v[82:85], v[60:63], v[214:217], v[82:85]
	v_mfma_f32_16x16x32_f16 v[120:123], v[60:63], v[226:229], v[120:123]
	v_mfma_f32_16x16x32_f16 v[124:127], v[242:245], v[214:217], v[124:127]
	v_mfma_f32_16x16x32_f16 v[146:149], v[242:245], v[218:221], v[146:149]
	v_mfma_f32_16x16x32_f16 v[134:137], v[242:245], v[226:229], v[134:137]
	v_mfma_f32_16x16x32_f16 v[138:141], v[60:63], v[218:221], v[138:141]
	v_mfma_f32_16x16x32_f16 v[142:145], v[60:63], v[222:225], v[142:145]
	v_mfma_f32_16x16x32_f16 v[150:153], v[242:245], v[222:225], v[150:153]
	s_setprio 0
	ds_read_b128 v[64:67], v130 offset:8192
	ds_read_b128 v[242:245], v130 offset:10240
	v_cvt_pk_f16_f32 v61, v72, v73
	v_cvt_pk_f16_f32 v60, v70, v71
	ds_write_b64 v100, v[60:61] offset:57344
	s_add_u32 s80, s22, 0xc0700
	s_addc_u32 s81, s90, 0
	global_load_dwordx4 v[60:63], v201, s[80:81] nt
	s_setprio 1
	s_waitcnt lgkmcnt(1)
	v_mfma_f32_16x16x32_f16 v[86:89], v[64:67], v[214:217], v[86:89]
	v_mfma_f32_16x16x32_f16 v[170:173], v[64:67], v[218:221], v[170:173]
	v_mfma_f32_16x16x32_f16 v[174:177], v[64:67], v[222:225], v[174:177]
	v_mfma_f32_16x16x32_f16 v[162:165], v[64:67], v[226:229], v[162:165]
	v_mfma_f32_16x16x32_f16 v[178:181], v[242:245], v[214:217], v[178:181]
	v_mfma_f32_16x16x32_f16 v[182:185], v[242:245], v[218:221], v[182:185]
	v_mfma_f32_16x16x32_f16 v[186:189], v[242:245], v[222:225], v[186:189]
	v_mfma_f32_16x16x32_f16 v[154:157], v[242:245], v[226:229], v[154:157]
	s_setprio 0
	ds_read_b128 v[64:67], v130 offset:12288
	ds_read_b128 v[68:71], v130 offset:14336
	v_cvt_pk_f16_f32 v39, v38, v39
	v_cvt_pk_f16_f32 v38, v36, v37
	ds_write_b64 v100, v[38:39] offset:61440
	s_add_u32 s80, s22, 0xe0700
	s_addc_u32 s81, s90, 0
	global_load_dwordx4 v[36:39], v201, s[80:81] nt
	s_setprio 1
	s_waitcnt lgkmcnt(1)
	v_mfma_f32_16x16x32_f16 v[90:93], v[64:67], v[218:221], v[90:93]
	v_mfma_f32_16x16x32_f16 v[242:245], v[64:67], v[214:217], v[74:77]
	v_mfma_f32_16x16x32_f16 v[158:161], v[64:67], v[222:225], v[158:161]
	v_mfma_f32_16x16x32_f16 v[166:169], v[64:67], v[226:229], v[166:169]
	v_mfma_f32_16x16x32_f16 v[190:193], v[68:71], v[214:217], v[190:193]
	v_mfma_f32_16x16x32_f16 v[202:205], v[68:71], v[218:221], v[202:205]
	v_mfma_f32_16x16x32_f16 v[206:209], v[68:71], v[222:225], v[206:209]
	v_mfma_f32_16x16x32_f16 v[210:213], v[68:71], v[226:229], v[210:213]
	s_setprio 0
	s_waitcnt vmcnt(4)
	s_waitcnt lgkmcnt(0)
	s_barrier
	ds_read_b128 v[214:217], v131 offset:32768
	ds_read_b128 v[218:221], v131 offset:34816
	ds_read_b128 v[222:225], v131 offset:36864
	ds_read_b128 v[226:229], v131 offset:38912
	ds_read_b128 v[64:67], v129 offset:32768
	ds_read_b128 v[68:71], v129 offset:34816
	s_add_u32 s80, s22, 0x800
	s_addc_u32 s81, s90, 0
	v_lshl_add_u64 v[198:199], s[38:39], 0, v[196:197]
	v_readfirstlane_b32 s1, v94
	s_mov_b32 m0, s1
	v_cvt_pk_f16_f32 v3, v2, v3
	global_load_lds_dwordx4 v[198:199], off
	v_cvt_pk_f16_f32 v2, v0, v1
	ds_write_b64 v100, v[2:3]
	global_load_dwordx4 v[0:3], v201, s[80:81] nt
	s_setprio 1
	s_waitcnt lgkmcnt(1)
	v_mfma_f32_16x16x32_f16 v[104:107], v[64:67], v[222:225], v[104:107]
	v_mfma_f32_16x16x32_f16 v[108:111], v[68:71], v[214:217], v[108:111]
	v_mfma_f32_16x16x32_f16 v[112:115], v[68:71], v[218:221], v[112:115]
	v_mfma_f32_16x16x32_f16 v[116:119], v[68:71], v[222:225], v[116:119]
	v_mfma_f32_16x16x32_f16 v[246:249], v[64:67], v[214:217], v[78:81]
	v_mfma_f32_16x16x32_f16 v[230:233], v[64:67], v[218:221], v[230:233]
	v_mfma_f32_16x16x32_f16 v[234:237], v[64:67], v[226:229], v[234:237]
	v_mfma_f32_16x16x32_f16 v[238:241], v[68:71], v[226:229], v[238:241]
	s_setprio 0
	ds_read_b128 v[68:71], v129 offset:36864
	ds_read_b128 v[72:75], v129 offset:38912
	v_readfirstlane_b32 s92, v99
	v_lshl_add_u64 v[64:65], v[198:199], 0, s[58:59]
	s_mov_b32 m0, s92
	v_cvt_pk_f16_f32 v11, v10, v11
	global_load_lds_dwordx4 v[64:65], off
	v_cvt_pk_f16_f32 v10, v8, v9
	ds_write_b64 v100, v[10:11] offset:4096
	s_add_u32 s80, s22, 0x20800
	s_addc_u32 s81, s90, 0
	global_load_dwordx4 v[64:67], v201, s[80:81] nt
	s_setprio 1
	s_waitcnt lgkmcnt(1)
	v_mfma_f32_16x16x32_f16 v[8:11], v[68:71], v[214:217], v[82:85]
	v_mfma_f32_16x16x32_f16 v[120:123], v[68:71], v[226:229], v[120:123]
	v_mfma_f32_16x16x32_f16 v[124:127], v[72:75], v[214:217], v[124:127]
	v_mfma_f32_16x16x32_f16 v[146:149], v[72:75], v[218:221], v[146:149]
	v_mfma_f32_16x16x32_f16 v[134:137], v[72:75], v[226:229], v[134:137]
	v_mfma_f32_16x16x32_f16 v[138:141], v[68:71], v[218:221], v[138:141]
	v_mfma_f32_16x16x32_f16 v[142:145], v[68:71], v[222:225], v[142:145]
	v_mfma_f32_16x16x32_f16 v[150:153], v[72:75], v[222:225], v[150:153]
	s_setprio 0
	ds_read_b128 v[72:75], v129 offset:40960
	ds_read_b128 v[76:79], v129 offset:43008
	v_readfirstlane_b32 s91, v101
	v_lshl_add_u64 v[68:69], v[198:199], 0, s[60:61]
	s_mov_b32 m0, s91
	v_cvt_pk_f16_f32 v15, v14, v15
	global_load_lds_dwordx4 v[68:69], off
	v_cvt_pk_f16_f32 v14, v12, v13
	ds_write_b64 v100, v[14:15] offset:8192
	s_add_u32 s80, s22, 0x40800
	s_addc_u32 s81, s90, 0
	global_load_dwordx4 v[68:71], v201, s[80:81] nt
	s_setprio 1
	s_waitcnt lgkmcnt(1)
	v_mfma_f32_16x16x32_f16 v[12:15], v[72:75], v[214:217], v[86:89]
	v_mfma_f32_16x16x32_f16 v[170:173], v[72:75], v[218:221], v[170:173]
	v_mfma_f32_16x16x32_f16 v[174:177], v[72:75], v[222:225], v[174:177]
	v_mfma_f32_16x16x32_f16 v[162:165], v[72:75], v[226:229], v[162:165]
	v_mfma_f32_16x16x32_f16 v[178:181], v[76:79], v[214:217], v[178:181]
	v_mfma_f32_16x16x32_f16 v[182:185], v[76:79], v[218:221], v[182:185]
	v_mfma_f32_16x16x32_f16 v[186:189], v[76:79], v[222:225], v[186:189]
	v_mfma_f32_16x16x32_f16 v[154:157], v[76:79], v[226:229], v[154:157]
	s_setprio 0
	ds_read_b128 v[76:79], v129 offset:45056
	ds_read_b128 v[80:83], v129 offset:47104
	v_readfirstlane_b32 s73, v102
	v_lshl_add_u64 v[72:73], v[198:199], 0, s[62:63]
	s_mov_b32 m0, s73
	v_cvt_pk_f16_f32 v19, v18, v19
	global_load_lds_dwordx4 v[72:73], off
	v_cvt_pk_f16_f32 v18, v16, v17
	ds_write_b64 v100, v[18:19] offset:12288
	s_add_u32 s80, s22, 0x60800
	s_addc_u32 s81, s90, 0
	global_load_dwordx4 v[72:75], v201, s[80:81] nt
	s_setprio 1
	s_waitcnt lgkmcnt(1)
	v_mfma_f32_16x16x32_f16 v[16:19], v[76:79], v[214:217], v[242:245]
	v_mfma_f32_16x16x32_f16 v[242:245], v[76:79], v[218:221], v[90:93]
	v_mfma_f32_16x16x32_f16 v[158:161], v[76:79], v[222:225], v[158:161]
	v_mfma_f32_16x16x32_f16 v[166:169], v[76:79], v[226:229], v[166:169]
	v_mfma_f32_16x16x32_f16 v[190:193], v[80:83], v[214:217], v[190:193]
	v_mfma_f32_16x16x32_f16 v[202:205], v[80:83], v[218:221], v[202:205]
	v_mfma_f32_16x16x32_f16 v[206:209], v[80:83], v[222:225], v[206:209]
	v_mfma_f32_16x16x32_f16 v[210:213], v[80:83], v[226:229], v[210:213]
	s_setprio 0
	ds_read_b128 v[214:217], v128 offset:32768
	ds_read_b128 v[218:221], v128 offset:34816
	ds_read_b128 v[222:225], v128 offset:36864
	ds_read_b128 v[226:229], v128 offset:38912
	ds_read_b128 v[80:83], v130 offset:32768
	ds_read_b128 v[84:87], v130 offset:34816
	v_cvt_pk_f16_f32 v23, v22, v23
	v_cvt_pk_f16_f32 v22, v20, v21
	ds_write_b64 v100, v[22:23] offset:16384
	s_add_u32 s80, s22, 0x80800
	s_addc_u32 s81, s90, 0
	global_load_dwordx4 v[76:79], v201, s[80:81] nt
	s_setprio 1
	s_waitcnt lgkmcnt(1)
	v_mfma_f32_16x16x32_f16 v[20:23], v[80:83], v[214:217], v[246:249]
	v_mfma_f32_16x16x32_f16 v[104:107], v[80:83], v[222:225], v[104:107]
	v_mfma_f32_16x16x32_f16 v[108:111], v[84:87], v[214:217], v[108:111]
	v_mfma_f32_16x16x32_f16 v[112:115], v[84:87], v[218:221], v[112:115]
	v_mfma_f32_16x16x32_f16 v[116:119], v[84:87], v[222:225], v[116:119]
	v_mfma_f32_16x16x32_f16 v[230:233], v[80:83], v[218:221], v[230:233]
	v_mfma_f32_16x16x32_f16 v[234:237], v[80:83], v[226:229], v[234:237]
	v_mfma_f32_16x16x32_f16 v[238:241], v[84:87], v[226:229], v[238:241]
	s_setprio 0
	ds_read_b128 v[84:87], v130 offset:36864
	ds_read_b128 v[88:91], v130 offset:38912
	v_cvt_pk_f16_f32 v27, v26, v27
	v_cvt_pk_f16_f32 v26, v24, v25
	ds_write_b64 v100, v[26:27] offset:20480
	s_add_u32 s80, s22, 0xa0800
	s_addc_u32 s81, s90, 0
	global_load_dwordx4 v[80:83], v201, s[80:81] nt
	s_setprio 1
	s_waitcnt lgkmcnt(1)
	v_mfma_f32_16x16x32_f16 v[24:27], v[84:87], v[214:217], v[8:11]
	v_mfma_f32_16x16x32_f16 v[120:123], v[84:87], v[226:229], v[120:123]
	v_mfma_f32_16x16x32_f16 v[124:127], v[88:91], v[214:217], v[124:127]
	v_mfma_f32_16x16x32_f16 v[146:149], v[88:91], v[218:221], v[146:149]
	v_mfma_f32_16x16x32_f16 v[134:137], v[88:91], v[226:229], v[134:137]
	v_mfma_f32_16x16x32_f16 v[138:141], v[84:87], v[218:221], v[138:141]
	v_mfma_f32_16x16x32_f16 v[142:145], v[84:87], v[222:225], v[142:145]
	v_mfma_f32_16x16x32_f16 v[150:153], v[88:91], v[222:225], v[150:153]
	s_setprio 0
	ds_read_b128 v[8:11], v130 offset:40960
	ds_read_b128 v[88:91], v130 offset:43008
	v_cvt_pk_f16_f32 v31, v30, v31
	v_cvt_pk_f16_f32 v30, v28, v29
	ds_write_b64 v100, v[30:31] offset:24576
	s_add_u32 s80, s22, 0xc0800
	s_addc_u32 s81, s90, 0
	global_load_dwordx4 v[84:87], v201, s[80:81] nt
	s_setprio 1
	s_waitcnt lgkmcnt(1)
	v_mfma_f32_16x16x32_f16 v[12:15], v[8:11], v[214:217], v[12:15]
	v_mfma_f32_16x16x32_f16 v[28:31], v[8:11], v[218:221], v[170:173]
	v_mfma_f32_16x16x32_f16 v[170:173], v[8:11], v[222:225], v[174:177]
	v_mfma_f32_16x16x32_f16 v[162:165], v[8:11], v[226:229], v[162:165]
	v_mfma_f32_16x16x32_f16 v[174:177], v[88:91], v[214:217], v[178:181]
	v_mfma_f32_16x16x32_f16 v[178:181], v[88:91], v[218:221], v[182:185]
	v_mfma_f32_16x16x32_f16 v[182:185], v[88:91], v[222:225], v[186:189]
	v_mfma_f32_16x16x32_f16 v[154:157], v[88:91], v[226:229], v[154:157]
	s_setprio 0
	ds_read_b128 v[8:11], v130 offset:45056
	ds_read_b128 v[186:189], v130 offset:47104
	v_cvt_pk_f16_f32 v35, v34, v35
	v_cvt_pk_f16_f32 v34, v32, v33
	ds_write_b64 v100, v[34:35] offset:28672
	s_add_u32 s80, s22, 0xe0800
	s_addc_u32 s81, s90, 0
	global_load_dwordx4 v[88:91], v201, s[80:81] nt
	s_setprio 1
	s_waitcnt lgkmcnt(1)
	v_mfma_f32_16x16x32_f16 v[16:19], v[8:11], v[214:217], v[16:19]
	v_mfma_f32_16x16x32_f16 v[32:35], v[8:11], v[218:221], v[242:245]
	v_mfma_f32_16x16x32_f16 v[158:161], v[8:11], v[222:225], v[158:161]
	v_mfma_f32_16x16x32_f16 v[166:169], v[8:11], v[226:229], v[166:169]
	v_mfma_f32_16x16x32_f16 v[190:193], v[186:189], v[214:217], v[190:193]
	v_mfma_f32_16x16x32_f16 v[202:205], v[186:189], v[218:221], v[202:205]
	v_mfma_f32_16x16x32_f16 v[206:209], v[186:189], v[222:225], v[206:209]
	v_mfma_f32_16x16x32_f16 v[186:189], v[186:189], v[226:229], v[210:213]
	s_setprio 0
	s_waitcnt vmcnt(4)
	s_waitcnt lgkmcnt(0)
	s_barrier
	s_nop 0
	ds_read_b128 v[210:213], v131
	ds_read_b128 v[214:217], v131 offset:2048
	ds_read_b128 v[218:221], v131 offset:4096
	ds_read_b128 v[222:225], v131 offset:6144
	ds_read_b128 v[8:11], v129
	ds_read_b128 v[226:229], v129 offset:2048
	s_add_u32 s80, s22, 0x900
	v_lshl_add_u64 v[92:93], s[40:41], 0, v[196:197]
	s_addc_u32 s81, s90, 0
	v_cvt_pk_f16_f32 v7, v6, v7
	s_cmp_lg_u32 s2, 0
	s_cbranch_scc1 .Lres_skip_0
	s_add_u32 m0, s0, 0x18000
	s_nop 0
	global_load_lds_dwordx4 v[92:93], off
.Lres_skip_0:
	v_cvt_pk_f16_f32 v6, v4, v5
	ds_write_b64 v100, v[6:7] offset:32768
	global_load_dwordx4 v[4:7], v201, s[80:81] nt
	s_setprio 1
	s_waitcnt lgkmcnt(1)
	v_mfma_f32_16x16x32_f16 v[20:23], v[8:11], v[210:213], v[20:23]
	v_mfma_f32_16x16x32_f16 v[104:107], v[8:11], v[218:221], v[104:107]
	v_mfma_f32_16x16x32_f16 v[108:111], v[226:229], v[210:213], v[108:111]
	v_mfma_f32_16x16x32_f16 v[112:115], v[226:229], v[214:217], v[112:115]
	v_mfma_f32_16x16x32_f16 v[116:119], v[226:229], v[218:221], v[116:119]
	v_mfma_f32_16x16x32_f16 v[230:233], v[8:11], v[214:217], v[230:233]
	v_mfma_f32_16x16x32_f16 v[234:237], v[8:11], v[222:225], v[234:237]
	v_mfma_f32_16x16x32_f16 v[226:229], v[226:229], v[222:225], v[238:241]
	s_setprio 0
	s_nop 1
	ds_read_b128 v[238:241], v129 offset:4096
	ds_read_b128 v[242:245], v129 offset:6144
	s_cmp_lg_u32 s2, 0
	s_cbranch_scc1 .Lres_skip_1
	s_add_u32 m0, s72, 0x18000
	s_nop 0
	v_lshl_add_u64 v[8:9], v[92:93], 0, s[58:59]
	global_load_lds_dwordx4 v[8:9], off
.Lres_skip_1:
	v_cvt_pk_f16_f32 v9, v42, v43
	v_cvt_pk_f16_f32 v8, v40, v41
	ds_write_b64 v100, v[8:9] offset:36864
	s_add_u32 s80, s22, 0x20900
	s_addc_u32 s81, s90, 0
	global_load_dwordx4 v[8:11], v201, s[80:81] nt
	s_setprio 1
	s_waitcnt lgkmcnt(1)
	v_mfma_f32_16x16x32_f16 v[24:27], v[238:241], v[210:213], v[24:27]
	v_mfma_f32_16x16x32_f16 v[120:123], v[238:241], v[222:225], v[120:123]
	v_mfma_f32_16x16x32_f16 v[124:127], v[242:245], v[210:213], v[124:127]
	v_mfma_f32_16x16x32_f16 v[146:149], v[242:245], v[214:217], v[146:149]
	v_mfma_f32_16x16x32_f16 v[134:137], v[242:245], v[222:225], v[134:137]
	v_mfma_f32_16x16x32_f16 v[138:141], v[238:241], v[214:217], v[138:141]
	v_mfma_f32_16x16x32_f16 v[142:145], v[238:241], v[218:221], v[142:145]
	v_mfma_f32_16x16x32_f16 v[150:153], v[242:245], v[218:221], v[150:153]
	s_setprio 0
	ds_read_b128 v[238:241], v129 offset:8192
	ds_read_b128 v[242:245], v129 offset:10240
	s_cmp_lg_u32 s2, 0
	s_cbranch_scc1 .Lres_skip_2
	s_add_u32 m0, s71, 0x18000
	s_nop 0
	v_lshl_add_u64 v[40:41], v[92:93], 0, s[60:61]
	global_load_lds_dwordx4 v[40:41], off
.Lres_skip_2:
	v_cvt_pk_f16_f32 v41, v46, v47
	v_cvt_pk_f16_f32 v40, v44, v45
	ds_write_b64 v100, v[40:41] offset:40960
	s_add_u32 s80, s22, 0x40900
	s_addc_u32 s81, s90, 0
	global_load_dwordx4 v[40:43], v201, s[80:81] nt
	s_setprio 1
	s_waitcnt lgkmcnt(1)
	v_mfma_f32_16x16x32_f16 v[12:15], v[238:241], v[210:213], v[12:15]
	v_mfma_f32_16x16x32_f16 v[28:31], v[238:241], v[214:217], v[28:31]
	v_mfma_f32_16x16x32_f16 v[170:173], v[238:241], v[218:221], v[170:173]
	v_mfma_f32_16x16x32_f16 v[162:165], v[238:241], v[222:225], v[162:165]
	v_mfma_f32_16x16x32_f16 v[174:177], v[242:245], v[210:213], v[174:177]
	v_mfma_f32_16x16x32_f16 v[178:181], v[242:245], v[214:217], v[178:181]
	v_mfma_f32_16x16x32_f16 v[182:185], v[242:245], v[218:221], v[182:185]
	v_mfma_f32_16x16x32_f16 v[154:157], v[242:245], v[222:225], v[154:157]
	s_setprio 0
	ds_read_b128 v[238:241], v129 offset:12288
	ds_read_b128 v[242:245], v129 offset:14336
	s_cmp_lg_u32 s2, 0
	s_cbranch_scc1 .Lres_skip_3
	s_add_u32 m0, s70, 0x18000
	s_nop 0
	v_lshl_add_u64 v[44:45], v[92:93], 0, s[62:63]
	global_load_lds_dwordx4 v[44:45], off
.Lres_skip_3:
	v_cvt_pk_f16_f32 v45, v50, v51
	v_cvt_pk_f16_f32 v44, v48, v49
	ds_write_b64 v100, v[44:45] offset:45056
	s_add_u32 s70, s22, 0x60900
	s_addc_u32 s71, s90, 0
	global_load_dwordx4 v[44:47], v201, s[70:71] nt
	s_setprio 1
	s_waitcnt lgkmcnt(1)
	v_mfma_f32_16x16x32_f16 v[16:19], v[238:241], v[210:213], v[16:19]
	v_mfma_f32_16x16x32_f16 v[32:35], v[238:241], v[214:217], v[32:35]
	v_mfma_f32_16x16x32_f16 v[158:161], v[238:241], v[218:221], v[158:161]
	v_mfma_f32_16x16x32_f16 v[166:169], v[238:241], v[222:225], v[166:169]
	v_mfma_f32_16x16x32_f16 v[190:193], v[242:245], v[210:213], v[190:193]
	v_mfma_f32_16x16x32_f16 v[202:205], v[242:245], v[214:217], v[202:205]
	v_mfma_f32_16x16x32_f16 v[206:209], v[242:245], v[218:221], v[206:209]
	v_mfma_f32_16x16x32_f16 v[186:189], v[242:245], v[222:225], v[186:189]
	s_setprio 0
	ds_read_b128 v[210:213], v128
	ds_read_b128 v[214:217], v128 offset:2048
	ds_read_b128 v[218:221], v128 offset:4096
	ds_read_b128 v[222:225], v128 offset:6144
	ds_read_b128 v[238:241], v130
	ds_read_b128 v[242:245], v130 offset:2048
	v_cvt_pk_f16_f32 v49, v54, v55
	v_cvt_pk_f16_f32 v48, v52, v53
	ds_write_b64 v100, v[48:49] offset:49152
	s_add_u32 s70, s22, 0x80900
	s_addc_u32 s71, s90, 0
	global_load_dwordx4 v[48:51], v201, s[70:71] nt
	s_setprio 1
	s_waitcnt lgkmcnt(1)
	v_mfma_f32_16x16x32_f16 v[20:23], v[238:241], v[210:213], v[20:23]
	v_mfma_f32_16x16x32_f16 v[104:107], v[238:241], v[218:221], v[104:107]
	v_mfma_f32_16x16x32_f16 v[108:111], v[242:245], v[210:213], v[108:111]
	v_mfma_f32_16x16x32_f16 v[112:115], v[242:245], v[214:217], v[112:115]
	v_mfma_f32_16x16x32_f16 v[116:119], v[242:245], v[218:221], v[116:119]
	v_mfma_f32_16x16x32_f16 v[230:233], v[238:241], v[214:217], v[230:233]
	v_mfma_f32_16x16x32_f16 v[234:237], v[238:241], v[222:225], v[234:237]
	v_mfma_f32_16x16x32_f16 v[226:229], v[242:245], v[222:225], v[226:229]
	s_setprio 0
	ds_read_b128 v[238:241], v130 offset:4096
	ds_read_b128 v[242:245], v130 offset:6144
	v_cvt_pk_f16_f32 v53, v58, v59
	v_cvt_pk_f16_f32 v52, v56, v57
	ds_write_b64 v100, v[52:53] offset:53248
	s_add_u32 s70, s22, 0xa0900
	s_addc_u32 s71, s90, 0
	global_load_dwordx4 v[52:55], v201, s[70:71] nt
	s_setprio 1
	s_waitcnt lgkmcnt(1)
	v_mfma_f32_16x16x32_f16 v[24:27], v[238:241], v[210:213], v[24:27]
	v_mfma_f32_16x16x32_f16 v[120:123], v[238:241], v[222:225], v[120:123]
	v_mfma_f32_16x16x32_f16 v[124:127], v[242:245], v[210:213], v[124:127]
	v_mfma_f32_16x16x32_f16 v[146:149], v[242:245], v[214:217], v[146:149]
	v_mfma_f32_16x16x32_f16 v[134:137], v[242:245], v[222:225], v[134:137]
	v_mfma_f32_16x16x32_f16 v[138:141], v[238:241], v[214:217], v[138:141]
	v_mfma_f32_16x16x32_f16 v[142:145], v[238:241], v[218:221], v[142:145]
	v_mfma_f32_16x16x32_f16 v[150:153], v[242:245], v[218:221], v[150:153]
	s_setprio 0
	ds_read_b128 v[238:241], v130 offset:8192
	ds_read_b128 v[242:245], v130 offset:10240
	v_cvt_pk_f16_f32 v57, v62, v63
	v_cvt_pk_f16_f32 v56, v60, v61
	ds_write_b64 v100, v[56:57] offset:57344
	s_add_u32 s70, s22, 0xc0900
	s_addc_u32 s71, s90, 0
	global_load_dwordx4 v[56:59], v201, s[70:71] nt
	s_setprio 1
	s_waitcnt lgkmcnt(1)
	v_mfma_f32_16x16x32_f16 v[28:31], v[238:241], v[214:217], v[28:31]
	v_mfma_f32_16x16x32_f16 v[246:249], v[238:241], v[210:213], v[12:15]
	v_mfma_f32_16x16x32_f16 v[170:173], v[238:241], v[218:221], v[170:173]
	v_mfma_f32_16x16x32_f16 v[162:165], v[238:241], v[222:225], v[162:165]
	v_mfma_f32_16x16x32_f16 v[174:177], v[242:245], v[210:213], v[174:177]
	v_mfma_f32_16x16x32_f16 v[178:181], v[242:245], v[214:217], v[178:181]
	v_mfma_f32_16x16x32_f16 v[182:185], v[242:245], v[218:221], v[182:185]
	v_mfma_f32_16x16x32_f16 v[154:157], v[242:245], v[222:225], v[154:157]
	s_setprio 0
	ds_read_b128 v[12:15], v130 offset:12288
	ds_read_b128 v[238:241], v130 offset:14336
	v_cvt_pk_f16_f32 v39, v38, v39
	v_cvt_pk_f16_f32 v38, v36, v37
	ds_write_b64 v100, v[38:39] offset:61440
	s_add_u32 s70, s22, 0xe0900
	s_addc_u32 s71, s90, 0
	global_load_dwordx4 v[60:63], v201, s[70:71] nt
	s_setprio 1
	s_waitcnt lgkmcnt(1)
	v_mfma_f32_16x16x32_f16 v[36:39], v[12:15], v[210:213], v[16:19]
	v_mfma_f32_16x16x32_f16 v[32:35], v[12:15], v[214:217], v[32:35]
	v_mfma_f32_16x16x32_f16 v[158:161], v[12:15], v[218:221], v[158:161]
	v_mfma_f32_16x16x32_f16 v[166:169], v[12:15], v[222:225], v[166:169]
	v_mfma_f32_16x16x32_f16 v[190:193], v[238:241], v[210:213], v[190:193]
	v_mfma_f32_16x16x32_f16 v[202:205], v[238:241], v[214:217], v[202:205]
	v_mfma_f32_16x16x32_f16 v[206:209], v[238:241], v[218:221], v[206:209]
	v_mfma_f32_16x16x32_f16 v[186:189], v[238:241], v[222:225], v[186:189]
	s_setprio 0
	s_waitcnt vmcnt(4)
	s_waitcnt lgkmcnt(0)
	s_barrier
	v_add_u32_e32 v250, 0x20000, v129
	v_add_u32_e32 v251, 0x20000, v130
	ds_read_b128 v[210:213], v131 offset:32768
	ds_read_b128 v[214:217], v131 offset:34816
	ds_read_b128 v[218:221], v131 offset:36864
	ds_read_b128 v[222:225], v131 offset:38912
	ds_read_b128 v[12:15], v250
	ds_read_b128 v[16:19], v250 offset:2048
	s_add_u32 s70, s22, 0xa00
	v_lshl_add_u64 v[92:93], s[42:43], 0, v[196:197]
	s_addc_u32 s71, s90, 0
	s_mov_b32 m0, s1
	v_cvt_pk_f16_f32 v3, v2, v3
	global_load_lds_dwordx4 v[92:93], off
	v_cvt_pk_f16_f32 v2, v0, v1
	ds_write_b64 v100, v[2:3]
	global_load_dwordx4 v[0:3], v201, s[70:71] nt
	s_setprio 1
	s_waitcnt lgkmcnt(1)
	v_mfma_f32_16x16x32_f16 v[104:107], v[12:15], v[218:221], v[104:107]
	v_mfma_f32_16x16x32_f16 v[108:111], v[16:19], v[210:213], v[108:111]
	v_mfma_f32_16x16x32_f16 v[112:115], v[16:19], v[214:217], v[112:115]
	v_mfma_f32_16x16x32_f16 v[116:119], v[16:19], v[218:221], v[116:119]
	v_mfma_f32_16x16x32_f16 v[238:241], v[12:15], v[210:213], v[20:23]
	v_mfma_f32_16x16x32_f16 v[230:233], v[12:15], v[214:217], v[230:233]
	v_mfma_f32_16x16x32_f16 v[234:237], v[12:15], v[222:225], v[234:237]
	v_mfma_f32_16x16x32_f16 v[226:229], v[16:19], v[222:225], v[226:229]
	s_setprio 0
	ds_read_b128 v[16:19], v250 offset:4096
	ds_read_b128 v[20:23], v250 offset:6144
	s_mov_b32 m0, s92
	v_lshl_add_u64 v[12:13], v[92:93], 0, s[58:59]
	global_load_lds_dwordx4 v[12:13], off
	v_cvt_pk_f16_f32 v13, v66, v67
	v_cvt_pk_f16_f32 v12, v64, v65
	ds_write_b64 v100, v[12:13] offset:4096
	s_add_u32 s0, s22, 0x20a00
	s_addc_u32 s1, s90, 0
	global_load_dwordx4 v[12:15], v201, s[0:1] nt
	s_setprio 1
	s_waitcnt lgkmcnt(1)
	v_mfma_f32_16x16x32_f16 v[64:67], v[16:19], v[210:213], v[24:27]
	v_mfma_f32_16x16x32_f16 v[120:123], v[16:19], v[222:225], v[120:123]
	v_mfma_f32_16x16x32_f16 v[124:127], v[20:23], v[210:213], v[124:127]
	v_mfma_f32_16x16x32_f16 v[146:149], v[20:23], v[214:217], v[146:149]
	v_mfma_f32_16x16x32_f16 v[134:137], v[20:23], v[222:225], v[134:137]
	v_mfma_f32_16x16x32_f16 v[138:141], v[16:19], v[214:217], v[138:141]
	v_mfma_f32_16x16x32_f16 v[142:145], v[16:19], v[218:221], v[142:145]
	v_mfma_f32_16x16x32_f16 v[150:153], v[20:23], v[218:221], v[150:153]
	s_setprio 0
	ds_read_b128 v[20:23], v250 offset:8192
	ds_read_b128 v[24:27], v250 offset:10240
	s_mov_b32 m0, s91
	v_lshl_add_u64 v[16:17], v[92:93], 0, s[60:61]
	global_load_lds_dwordx4 v[16:17], off
	v_cvt_pk_f16_f32 v17, v70, v71
	v_cvt_pk_f16_f32 v16, v68, v69
	ds_write_b64 v100, v[16:17] offset:8192
	s_add_u32 s0, s22, 0x40a00
	s_addc_u32 s1, s90, 0
	global_load_dwordx4 v[16:19], v201, s[0:1] nt
	s_setprio 1
	s_waitcnt lgkmcnt(1)
	v_mfma_f32_16x16x32_f16 v[68:71], v[20:23], v[210:213], v[246:249]
	v_mfma_f32_16x16x32_f16 v[242:245], v[20:23], v[214:217], v[28:31]
	v_mfma_f32_16x16x32_f16 v[170:173], v[20:23], v[218:221], v[170:173]
	v_mfma_f32_16x16x32_f16 v[162:165], v[20:23], v[222:225], v[162:165]
	v_mfma_f32_16x16x32_f16 v[174:177], v[24:27], v[210:213], v[174:177]
	v_mfma_f32_16x16x32_f16 v[178:181], v[24:27], v[214:217], v[178:181]
	v_mfma_f32_16x16x32_f16 v[182:185], v[24:27], v[218:221], v[182:185]
	v_mfma_f32_16x16x32_f16 v[154:157], v[24:27], v[222:225], v[154:157]
	s_setprio 0
	ds_read_b128 v[24:27], v250 offset:12288
	ds_read_b128 v[28:31], v250 offset:14336
	s_mov_b32 m0, s73
	v_lshl_add_u64 v[20:21], v[92:93], 0, s[62:63]
	global_load_lds_dwordx4 v[20:21], off
	v_cvt_pk_f16_f32 v21, v74, v75
	v_cvt_pk_f16_f32 v20, v72, v73
	ds_write_b64 v100, v[20:21] offset:12288
	s_add_u32 s0, s22, 0x60a00
	s_addc_u32 s1, s90, 0
	global_load_dwordx4 v[20:23], v201, s[0:1] nt
	s_setprio 1
	s_waitcnt lgkmcnt(1)
	v_mfma_f32_16x16x32_f16 v[72:75], v[24:27], v[210:213], v[36:39]
	v_mfma_f32_16x16x32_f16 v[246:249], v[24:27], v[214:217], v[32:35]
	v_mfma_f32_16x16x32_f16 v[158:161], v[24:27], v[218:221], v[158:161]
	v_mfma_f32_16x16x32_f16 v[166:169], v[24:27], v[222:225], v[166:169]
	v_mfma_f32_16x16x32_f16 v[190:193], v[28:31], v[210:213], v[190:193]
	v_mfma_f32_16x16x32_f16 v[202:205], v[28:31], v[214:217], v[202:205]
	v_mfma_f32_16x16x32_f16 v[206:209], v[28:31], v[218:221], v[206:209]
	v_mfma_f32_16x16x32_f16 v[186:189], v[28:31], v[222:225], v[186:189]
	s_setprio 0
	ds_read_b128 v[210:213], v128 offset:32768
	ds_read_b128 v[214:217], v128 offset:34816
	ds_read_b128 v[218:221], v128 offset:36864
	ds_read_b128 v[222:225], v128 offset:38912
	ds_read_b128 v[28:31], v251
	ds_read_b128 v[32:35], v251 offset:2048
	v_cvt_pk_f16_f32 v25, v78, v79
	v_cvt_pk_f16_f32 v24, v76, v77
	ds_write_b64 v100, v[24:25] offset:16384
	s_add_u32 s0, s22, 0x80a00
	s_addc_u32 s1, s90, 0
	global_load_dwordx4 v[24:27], v201, s[0:1] nt
	s_setprio 1
	s_waitcnt lgkmcnt(1)
	v_mfma_f32_16x16x32_f16 v[76:79], v[28:31], v[210:213], v[238:241]
	v_mfma_f32_16x16x32_f16 v[104:107], v[28:31], v[218:221], v[104:107]
	v_mfma_f32_16x16x32_f16 v[108:111], v[32:35], v[210:213], v[108:111]
	v_mfma_f32_16x16x32_f16 v[112:115], v[32:35], v[214:217], v[112:115]
	v_mfma_f32_16x16x32_f16 v[116:119], v[32:35], v[218:221], v[116:119]
	v_mfma_f32_16x16x32_f16 v[230:233], v[28:31], v[214:217], v[230:233]
	v_mfma_f32_16x16x32_f16 v[234:237], v[28:31], v[222:225], v[234:237]
	v_mfma_f32_16x16x32_f16 v[226:229], v[32:35], v[222:225], v[226:229]
	s_setprio 0
	ds_read_b128 v[32:35], v251 offset:4096
	ds_read_b128 v[36:39], v251 offset:6144
	v_cvt_pk_f16_f32 v29, v82, v83
	v_cvt_pk_f16_f32 v28, v80, v81
	ds_write_b64 v100, v[28:29] offset:20480
	s_add_u32 s0, s22, 0xa0a00
	s_addc_u32 s1, s90, 0
	global_load_dwordx4 v[28:31], v201, s[0:1] nt
	s_setprio 1
	s_waitcnt lgkmcnt(1)
	v_mfma_f32_16x16x32_f16 v[80:83], v[32:35], v[210:213], v[64:67]
	v_mfma_f32_16x16x32_f16 v[120:123], v[32:35], v[222:225], v[120:123]
	v_mfma_f32_16x16x32_f16 v[124:127], v[36:39], v[210:213], v[124:127]
	v_mfma_f32_16x16x32_f16 v[146:149], v[36:39], v[214:217], v[146:149]
	v_mfma_f32_16x16x32_f16 v[134:137], v[36:39], v[222:225], v[134:137]
	v_mfma_f32_16x16x32_f16 v[138:141], v[32:35], v[214:217], v[138:141]
	v_mfma_f32_16x16x32_f16 v[142:145], v[32:35], v[218:221], v[142:145]
	v_mfma_f32_16x16x32_f16 v[150:153], v[36:39], v[218:221], v[150:153]
	s_setprio 0
	ds_read_b128 v[36:39], v251 offset:8192
	ds_read_b128 v[64:67], v251 offset:10240
	v_cvt_pk_f16_f32 v33, v86, v87
	v_cvt_pk_f16_f32 v32, v84, v85
	ds_write_b64 v100, v[32:33] offset:24576
	s_add_u32 s0, s22, 0xc0a00
	s_addc_u32 s1, s90, 0
	global_load_dwordx4 v[32:35], v201, s[0:1] nt
	s_setprio 1
	s_waitcnt lgkmcnt(1)
	v_mfma_f32_16x16x32_f16 v[68:71], v[36:39], v[210:213], v[68:71]
	v_mfma_f32_16x16x32_f16 v[84:87], v[36:39], v[214:217], v[242:245]
	v_mfma_f32_16x16x32_f16 v[170:173], v[36:39], v[218:221], v[170:173]
	v_mfma_f32_16x16x32_f16 v[162:165], v[36:39], v[222:225], v[162:165]
	v_mfma_f32_16x16x32_f16 v[174:177], v[64:67], v[210:213], v[174:177]
	v_mfma_f32_16x16x32_f16 v[178:181], v[64:67], v[214:217], v[178:181]
	v_mfma_f32_16x16x32_f16 v[182:185], v[64:67], v[218:221], v[182:185]
	v_mfma_f32_16x16x32_f16 v[154:157], v[64:67], v[222:225], v[154:157]
	s_setprio 0
	ds_read_b128 v[64:67], v251 offset:12288
	ds_read_b128 v[238:241], v251 offset:14336
	v_cvt_pk_f16_f32 v37, v90, v91
	v_cvt_pk_f16_f32 v36, v88, v89
	ds_write_b64 v100, v[36:37] offset:28672
	s_add_u32 s0, s22, 0xe0a00
	s_addc_u32 s1, s90, 0
	global_load_dwordx4 v[36:39], v201, s[0:1] nt
	s_setprio 1
	s_waitcnt lgkmcnt(1)
	v_mfma_f32_16x16x32_f16 v[72:75], v[64:67], v[210:213], v[72:75]
	v_mfma_f32_16x16x32_f16 v[88:91], v[64:67], v[214:217], v[246:249]
	v_mfma_f32_16x16x32_f16 v[158:161], v[64:67], v[218:221], v[158:161]
	v_mfma_f32_16x16x32_f16 v[166:169], v[64:67], v[222:225], v[166:169]
	v_mfma_f32_16x16x32_f16 v[190:193], v[238:241], v[210:213], v[190:193]
	v_mfma_f32_16x16x32_f16 v[202:205], v[238:241], v[214:217], v[202:205]
	v_mfma_f32_16x16x32_f16 v[206:209], v[238:241], v[218:221], v[206:209]
	v_mfma_f32_16x16x32_f16 v[186:189], v[238:241], v[222:225], v[186:189]
	s_setprio 0
	s_waitcnt vmcnt(4)
	s_waitcnt lgkmcnt(0)
	s_barrier
	ds_read_b128 v[210:213], v131
	ds_read_b128 v[214:217], v131 offset:2048
	ds_read_b128 v[218:221], v131 offset:4096
	ds_read_b128 v[222:225], v131 offset:6144
	ds_read_b128 v[64:67], v129
	ds_read_b128 v[238:241], v129 offset:2048
	s_add_u32 s70, s22, 0xb00
	v_lshl_add_u64 v[92:93], s[44:45], 0, v[196:197]
	s_addc_u32 s71, s90, 0
	v_readfirstlane_b32 s0, v95
	s_mov_b32 m0, s0
	v_cvt_pk_f16_f32 v7, v6, v7
	global_load_lds_dwordx4 v[92:93], off
	v_cvt_pk_f16_f32 v6, v4, v5
	ds_write_b64 v100, v[6:7] offset:32768
	global_load_dwordx4 v[4:7], v201, s[70:71] nt
	s_setprio 1
	s_waitcnt lgkmcnt(1)
	v_mfma_f32_16x16x32_f16 v[76:79], v[64:67], v[210:213], v[76:79]
	v_mfma_f32_16x16x32_f16 v[104:107], v[64:67], v[218:221], v[104:107]
	v_mfma_f32_16x16x32_f16 v[108:111], v[238:241], v[210:213], v[108:111]
	v_mfma_f32_16x16x32_f16 v[112:115], v[238:241], v[214:217], v[112:115]
	v_mfma_f32_16x16x32_f16 v[116:119], v[238:241], v[218:221], v[116:119]
	v_mfma_f32_16x16x32_f16 v[230:233], v[64:67], v[214:217], v[230:233]
	v_mfma_f32_16x16x32_f16 v[234:237], v[64:67], v[222:225], v[234:237]
	v_mfma_f32_16x16x32_f16 v[226:229], v[238:241], v[222:225], v[226:229]
	s_setprio 0
	ds_read_b128 v[238:241], v129 offset:4096
	ds_read_b128 v[242:245], v129 offset:6144
	v_readfirstlane_b32 s72, v96
	v_lshl_add_u64 v[64:65], v[92:93], 0, s[58:59]
	s_mov_b32 m0, s72
	v_cvt_pk_f16_f32 v11, v10, v11
	global_load_lds_dwordx4 v[64:65], off
	v_cvt_pk_f16_f32 v10, v8, v9
	ds_write_b64 v100, v[10:11] offset:36864
	s_add_u32 s70, s22, 0x20b00
	s_addc_u32 s71, s90, 0
	global_load_dwordx4 v[64:67], v201, s[70:71] nt
	s_setprio 1
	s_waitcnt lgkmcnt(1)
	v_mfma_f32_16x16x32_f16 v[8:11], v[238:241], v[210:213], v[80:83]
	v_mfma_f32_16x16x32_f16 v[80:83], v[238:241], v[214:217], v[138:141]
	v_mfma_f32_16x16x32_f16 v[138:141], v[238:241], v[218:221], v[142:145]
	v_mfma_f32_16x16x32_f16 v[120:123], v[238:241], v[222:225], v[120:123]
	v_mfma_f32_16x16x32_f16 v[124:127], v[242:245], v[210:213], v[124:127]
	v_mfma_f32_16x16x32_f16 v[142:145], v[242:245], v[214:217], v[146:149]
	v_mfma_f32_16x16x32_f16 v[146:149], v[242:245], v[218:221], v[150:153]
	v_mfma_f32_16x16x32_f16 v[134:137], v[242:245], v[222:225], v[134:137]
	s_setprio 0
	s_nop 0
	ds_read_b128 v[150:153], v129 offset:8192
	ds_read_b128 v[238:241], v129 offset:10240
	v_readfirstlane_b32 s71, v97
	v_lshl_add_u64 v[198:199], v[92:93], 0, s[60:61]
	s_mov_b32 m0, s71
	v_cvt_pk_f16_f32 v43, v42, v43
	global_load_lds_dwordx4 v[198:199], off
	v_cvt_pk_f16_f32 v42, v40, v41
	ds_write_b64 v100, v[42:43] offset:40960
	s_add_u32 s80, s22, 0x40b00
	s_addc_u32 s81, s90, 0
	global_load_dwordx4 v[40:43], v201, s[80:81] nt
	s_setprio 1
	s_waitcnt lgkmcnt(1)
	v_mfma_f32_16x16x32_f16 v[68:71], v[150:153], v[210:213], v[68:71]
	v_mfma_f32_16x16x32_f16 v[84:87], v[150:153], v[214:217], v[84:87]
	v_mfma_f32_16x16x32_f16 v[170:173], v[150:153], v[218:221], v[170:173]
	v_mfma_f32_16x16x32_f16 v[150:153], v[150:153], v[222:225], v[162:165]
	v_mfma_f32_16x16x32_f16 v[162:165], v[238:241], v[210:213], v[174:177]
	v_mfma_f32_16x16x32_f16 v[174:177], v[238:241], v[214:217], v[178:181]
	v_mfma_f32_16x16x32_f16 v[178:181], v[238:241], v[218:221], v[182:185]
	v_mfma_f32_16x16x32_f16 v[154:157], v[238:241], v[222:225], v[154:157]
	s_setprio 0
	s_nop 0
	ds_read_b128 v[182:185], v129 offset:12288
	ds_read_b128 v[238:241], v129 offset:14336
	v_readfirstlane_b32 s70, v98
	v_lshl_add_u64 v[92:93], v[92:93], 0, s[62:63]
	s_mov_b32 m0, s70
	v_cvt_pk_f16_f32 v47, v46, v47
	global_load_lds_dwordx4 v[92:93], off
	v_cvt_pk_f16_f32 v46, v44, v45
	ds_write_b64 v100, v[46:47] offset:45056
	s_add_u32 s80, s22, 0x60b00
	s_addc_u32 s81, s90, 0
	global_load_dwordx4 v[44:47], v201, s[80:81] nt
	s_setprio 1
	s_waitcnt lgkmcnt(1)
	v_mfma_f32_16x16x32_f16 v[72:75], v[182:185], v[210:213], v[72:75]
	v_mfma_f32_16x16x32_f16 v[88:91], v[182:185], v[214:217], v[88:91]
	v_mfma_f32_16x16x32_f16 v[158:161], v[182:185], v[218:221], v[158:161]
	v_mfma_f32_16x16x32_f16 v[166:169], v[182:185], v[222:225], v[166:169]
	v_mfma_f32_16x16x32_f16 v[182:185], v[238:241], v[210:213], v[190:193]
	v_mfma_f32_16x16x32_f16 v[190:193], v[238:241], v[214:217], v[202:205]
	v_mfma_f32_16x16x32_f16 v[202:205], v[238:241], v[218:221], v[206:209]
	v_mfma_f32_16x16x32_f16 v[186:189], v[238:241], v[222:225], v[186:189]
	s_setprio 0
	s_nop 0
	ds_read_b128 v[206:209], v128
	ds_read_b128 v[210:213], v128 offset:2048
	ds_read_b128 v[214:217], v128 offset:4096
	ds_read_b128 v[218:221], v128 offset:6144
	ds_read_b128 v[222:225], v130
	ds_read_b128 v[238:241], v130 offset:2048
	v_cvt_pk_f16_f32 v51, v50, v51
	v_cvt_pk_f16_f32 v50, v48, v49
	ds_write_b64 v100, v[50:51] offset:49152
	s_add_u32 s80, s22, 0x80b00
	s_addc_u32 s81, s90, 0
	global_load_dwordx4 v[48:51], v201, s[80:81] nt
	s_setprio 1
	s_waitcnt lgkmcnt(1)
	v_mfma_f32_16x16x32_f16 v[76:79], v[222:225], v[206:209], v[76:79]
	v_mfma_f32_16x16x32_f16 v[104:107], v[222:225], v[214:217], v[104:107]
	v_mfma_f32_16x16x32_f16 v[108:111], v[238:241], v[206:209], v[108:111]
	v_mfma_f32_16x16x32_f16 v[112:115], v[238:241], v[210:213], v[112:115]
	v_mfma_f32_16x16x32_f16 v[116:119], v[238:241], v[214:217], v[116:119]
	v_mfma_f32_16x16x32_f16 v[230:233], v[222:225], v[210:213], v[230:233]
	v_mfma_f32_16x16x32_f16 v[222:225], v[222:225], v[218:221], v[234:237]
	v_mfma_f32_16x16x32_f16 v[226:229], v[238:241], v[218:221], v[226:229]
	s_setprio 0
	s_nop 0
	ds_read_b128 v[234:237], v130 offset:4096
	ds_read_b128 v[238:241], v130 offset:6144
	v_cvt_pk_f16_f32 v55, v54, v55
	v_cvt_pk_f16_f32 v54, v52, v53
	ds_write_b64 v100, v[54:55] offset:53248
	s_add_u32 s80, s22, 0xa0b00
	s_addc_u32 s81, s90, 0
	global_load_dwordx4 v[52:55], v201, s[80:81] nt
	s_setprio 1
	s_waitcnt lgkmcnt(1)
	v_mfma_f32_16x16x32_f16 v[80:83], v[234:237], v[210:213], v[80:83]
	v_mfma_f32_16x16x32_f16 v[120:123], v[234:237], v[218:221], v[120:123]
	v_mfma_f32_16x16x32_f16 v[124:127], v[238:241], v[206:209], v[124:127]
	v_mfma_f32_16x16x32_f16 v[146:149], v[238:241], v[214:217], v[146:149]
	v_mfma_f32_16x16x32_f16 v[134:137], v[238:241], v[218:221], v[134:137]
	v_mfma_f32_16x16x32_f16 v[242:245], v[234:237], v[206:209], v[8:11]
	v_mfma_f32_16x16x32_f16 v[138:141], v[234:237], v[214:217], v[138:141]
	v_mfma_f32_16x16x32_f16 v[142:145], v[238:241], v[210:213], v[142:145]
	s_setprio 0
	ds_read_b128 v[8:11], v130 offset:8192
	ds_read_b128 v[234:237], v130 offset:10240
	v_cvt_pk_f16_f32 v59, v58, v59
	v_cvt_pk_f16_f32 v58, v56, v57
	ds_write_b64 v100, v[58:59] offset:57344
	s_add_u32 s80, s22, 0xc0b00
	s_addc_u32 s81, s90, 0
	global_load_dwordx4 v[56:59], v201, s[80:81] nt
	s_setprio 1
	s_waitcnt lgkmcnt(1)
	v_mfma_f32_16x16x32_f16 v[84:87], v[8:11], v[210:213], v[84:87]
	v_mfma_f32_16x16x32_f16 v[238:241], v[8:11], v[206:209], v[68:71]
	v_mfma_f32_16x16x32_f16 v[170:173], v[8:11], v[214:217], v[170:173]
	v_mfma_f32_16x16x32_f16 v[150:153], v[8:11], v[218:221], v[150:153]
	v_mfma_f32_16x16x32_f16 v[162:165], v[234:237], v[206:209], v[162:165]
	v_mfma_f32_16x16x32_f16 v[174:177], v[234:237], v[210:213], v[174:177]
	v_mfma_f32_16x16x32_f16 v[178:181], v[234:237], v[214:217], v[178:181]
	v_mfma_f32_16x16x32_f16 v[154:157], v[234:237], v[218:221], v[154:157]
	s_setprio 0
	ds_read_b128 v[8:11], v130 offset:12288
	ds_read_b128 v[68:71], v130 offset:14336
	v_cvt_pk_f16_f32 v63, v62, v63
	v_cvt_pk_f16_f32 v62, v60, v61
	ds_write_b64 v100, v[62:63] offset:61440
	s_add_u32 s80, s22, 0xe0b00
	s_addc_u32 s81, s90, 0
	global_load_dwordx4 v[60:63], v201, s[80:81] nt
	s_setprio 1
	s_waitcnt lgkmcnt(1)
	v_mfma_f32_16x16x32_f16 v[88:91], v[8:11], v[210:213], v[88:91]
	v_mfma_f32_16x16x32_f16 v[234:237], v[8:11], v[206:209], v[72:75]
	v_mfma_f32_16x16x32_f16 v[158:161], v[8:11], v[214:217], v[158:161]
	v_mfma_f32_16x16x32_f16 v[166:169], v[8:11], v[218:221], v[166:169]
	v_mfma_f32_16x16x32_f16 v[182:185], v[68:71], v[206:209], v[182:185]
	v_mfma_f32_16x16x32_f16 v[190:193], v[68:71], v[210:213], v[190:193]
	v_mfma_f32_16x16x32_f16 v[202:205], v[68:71], v[214:217], v[202:205]
	v_mfma_f32_16x16x32_f16 v[186:189], v[68:71], v[218:221], v[186:189]
	s_setprio 0
	s_waitcnt vmcnt(4)
	s_waitcnt lgkmcnt(0)
	s_barrier
	ds_read_b128 v[206:209], v131 offset:32768
	ds_read_b128 v[210:213], v131 offset:34816
	ds_read_b128 v[214:217], v131 offset:36864
	ds_read_b128 v[218:221], v131 offset:38912
	ds_read_b128 v[68:71], v129 offset:32768
	ds_read_b128 v[72:75], v129 offset:34816
	s_add_u32 s80, s22, 0xc00
	v_lshl_add_u64 v[92:93], s[46:47], 0, v[196:197]
	s_addc_u32 s81, s90, 0
	v_readfirstlane_b32 s1, v94
	s_mov_b32 m0, s1
	v_cvt_pk_f16_f32 v3, v2, v3
	global_load_lds_dwordx4 v[92:93], off
	v_cvt_pk_f16_f32 v2, v0, v1
	ds_write_b64 v100, v[2:3]
	global_load_dwordx4 v[8:11], v201, s[80:81] nt
	s_setprio 1
	s_waitcnt lgkmcnt(1)
	v_mfma_f32_16x16x32_f16 v[0:3], v[68:71], v[206:209], v[76:79]
	v_mfma_f32_16x16x32_f16 v[104:107], v[68:71], v[214:217], v[104:107]
	v_mfma_f32_16x16x32_f16 v[108:111], v[72:75], v[206:209], v[108:111]
	v_mfma_f32_16x16x32_f16 v[112:115], v[72:75], v[210:213], v[112:115]
	v_mfma_f32_16x16x32_f16 v[116:119], v[72:75], v[214:217], v[116:119]
	v_mfma_f32_16x16x32_f16 v[230:233], v[68:71], v[210:213], v[230:233]
	v_mfma_f32_16x16x32_f16 v[222:225], v[68:71], v[218:221], v[222:225]
	v_mfma_f32_16x16x32_f16 v[226:229], v[72:75], v[218:221], v[226:229]
	s_setprio 0
	ds_read_b128 v[72:75], v129 offset:36864
	ds_read_b128 v[76:79], v129 offset:38912
	v_readfirstlane_b32 s92, v99
	v_lshl_add_u64 v[68:69], v[92:93], 0, s[58:59]
	s_mov_b32 m0, s92
	v_cvt_pk_f16_f32 v15, v14, v15
	global_load_lds_dwordx4 v[68:69], off
	v_cvt_pk_f16_f32 v14, v12, v13
	ds_write_b64 v100, v[14:15] offset:4096
	s_add_u32 s80, s22, 0x20c00
	s_addc_u32 s81, s90, 0
	global_load_dwordx4 v[68:71], v201, s[80:81] nt
	s_setprio 1
	s_waitcnt lgkmcnt(1)
	v_mfma_f32_16x16x32_f16 v[12:15], v[72:75], v[206:209], v[242:245]
	v_mfma_f32_16x16x32_f16 v[120:123], v[72:75], v[218:221], v[120:123]
	v_mfma_f32_16x16x32_f16 v[124:127], v[76:79], v[206:209], v[124:127]
	v_mfma_f32_16x16x32_f16 v[146:149], v[76:79], v[214:217], v[146:149]
	v_mfma_f32_16x16x32_f16 v[134:137], v[76:79], v[218:221], v[134:137]
	v_mfma_f32_16x16x32_f16 v[242:245], v[72:75], v[210:213], v[80:83]
	v_mfma_f32_16x16x32_f16 v[138:141], v[72:75], v[214:217], v[138:141]
	v_mfma_f32_16x16x32_f16 v[142:145], v[76:79], v[210:213], v[142:145]
	s_setprio 0
	ds_read_b128 v[76:79], v129 offset:40960
	ds_read_b128 v[80:83], v129 offset:43008
	v_readfirstlane_b32 s91, v101
	v_lshl_add_u64 v[72:73], v[92:93], 0, s[60:61]
	s_mov_b32 m0, s91
	v_cvt_pk_f16_f32 v19, v18, v19
	global_load_lds_dwordx4 v[72:73], off
	v_cvt_pk_f16_f32 v18, v16, v17
	ds_write_b64 v100, v[18:19] offset:8192
	s_add_u32 s80, s22, 0x40c00
	s_addc_u32 s81, s90, 0
	global_load_dwordx4 v[72:75], v201, s[80:81] nt
	s_setprio 1
	s_waitcnt lgkmcnt(1)
	v_mfma_f32_16x16x32_f16 v[16:19], v[76:79], v[206:209], v[238:241]
	v_mfma_f32_16x16x32_f16 v[238:241], v[76:79], v[210:213], v[84:87]
	v_mfma_f32_16x16x32_f16 v[170:173], v[76:79], v[214:217], v[170:173]
	v_mfma_f32_16x16x32_f16 v[150:153], v[76:79], v[218:221], v[150:153]
	v_mfma_f32_16x16x32_f16 v[162:165], v[80:83], v[206:209], v[162:165]
	v_mfma_f32_16x16x32_f16 v[174:177], v[80:83], v[210:213], v[174:177]
	v_mfma_f32_16x16x32_f16 v[178:181], v[80:83], v[214:217], v[178:181]
	v_mfma_f32_16x16x32_f16 v[154:157], v[80:83], v[218:221], v[154:157]
	s_setprio 0
	ds_read_b128 v[80:83], v129 offset:45056
	ds_read_b128 v[84:87], v129 offset:47104
	v_readfirstlane_b32 s73, v102
	v_lshl_add_u64 v[76:77], v[92:93], 0, s[62:63]
	s_mov_b32 m0, s73
	v_cvt_pk_f16_f32 v23, v22, v23
	global_load_lds_dwordx4 v[76:77], off
	v_cvt_pk_f16_f32 v22, v20, v21
	ds_write_b64 v100, v[22:23] offset:12288
	s_add_u32 s80, s22, 0x60c00
	s_addc_u32 s81, s90, 0
	global_load_dwordx4 v[76:79], v201, s[80:81] nt
	s_setprio 1
	s_waitcnt lgkmcnt(1)
	v_mfma_f32_16x16x32_f16 v[20:23], v[80:83], v[206:209], v[234:237]
	v_mfma_f32_16x16x32_f16 v[234:237], v[80:83], v[210:213], v[88:91]
	v_mfma_f32_16x16x32_f16 v[158:161], v[80:83], v[214:217], v[158:161]
	v_mfma_f32_16x16x32_f16 v[166:169], v[80:83], v[218:221], v[166:169]
	v_mfma_f32_16x16x32_f16 v[182:185], v[84:87], v[206:209], v[182:185]
	v_mfma_f32_16x16x32_f16 v[190:193], v[84:87], v[210:213], v[190:193]
	v_mfma_f32_16x16x32_f16 v[202:205], v[84:87], v[214:217], v[202:205]
	v_mfma_f32_16x16x32_f16 v[186:189], v[84:87], v[218:221], v[186:189]
	s_setprio 0
	ds_read_b128 v[206:209], v128 offset:32768
	ds_read_b128 v[210:213], v128 offset:34816
	ds_read_b128 v[214:217], v128 offset:36864
	ds_read_b128 v[218:221], v128 offset:38912
	ds_read_b128 v[84:87], v130 offset:32768
	ds_read_b128 v[88:91], v130 offset:34816
	v_cvt_pk_f16_f32 v27, v26, v27
	v_cvt_pk_f16_f32 v26, v24, v25
	ds_write_b64 v100, v[26:27] offset:16384
	s_add_u32 s80, s22, 0x80c00
	s_addc_u32 s81, s90, 0
	global_load_dwordx4 v[80:83], v201, s[80:81] nt
	s_setprio 1
	s_waitcnt lgkmcnt(1)
	v_mfma_f32_16x16x32_f16 v[24:27], v[84:87], v[206:209], v[0:3]
	v_mfma_f32_16x16x32_f16 v[104:107], v[84:87], v[214:217], v[104:107]
	v_mfma_f32_16x16x32_f16 v[108:111], v[88:91], v[206:209], v[108:111]
	v_mfma_f32_16x16x32_f16 v[112:115], v[88:91], v[210:213], v[112:115]
	v_mfma_f32_16x16x32_f16 v[116:119], v[88:91], v[214:217], v[116:119]
	v_mfma_f32_16x16x32_f16 v[230:233], v[84:87], v[210:213], v[230:233]
	v_mfma_f32_16x16x32_f16 v[222:225], v[84:87], v[218:221], v[222:225]
	v_mfma_f32_16x16x32_f16 v[226:229], v[88:91], v[218:221], v[226:229]
	s_setprio 0
	ds_read_b128 v[0:3], v130 offset:36864
	ds_read_b128 v[88:91], v130 offset:38912
	v_cvt_pk_f16_f32 v31, v30, v31
	v_cvt_pk_f16_f32 v30, v28, v29
	ds_write_b64 v100, v[30:31] offset:20480
	s_add_u32 s80, s22, 0xa0c00
	s_addc_u32 s81, s90, 0
	global_load_dwordx4 v[84:87], v201, s[80:81] nt
	s_setprio 1
	s_waitcnt lgkmcnt(1)
	v_mfma_f32_16x16x32_f16 v[12:15], v[0:3], v[206:209], v[12:15]
	v_mfma_f32_16x16x32_f16 v[28:31], v[0:3], v[210:213], v[242:245]
	v_mfma_f32_16x16x32_f16 v[120:123], v[0:3], v[218:221], v[120:123]
	v_mfma_f32_16x16x32_f16 v[124:127], v[88:91], v[206:209], v[124:127]
	v_mfma_f32_16x16x32_f16 v[146:149], v[88:91], v[214:217], v[146:149]
	v_mfma_f32_16x16x32_f16 v[134:137], v[88:91], v[218:221], v[134:137]
	v_mfma_f32_16x16x32_f16 v[138:141], v[0:3], v[214:217], v[138:141]
	v_mfma_f32_16x16x32_f16 v[142:145], v[88:91], v[210:213], v[142:145]
	s_setprio 0
	ds_read_b128 v[0:3], v130 offset:40960
	ds_read_b128 v[242:245], v130 offset:43008
	v_cvt_pk_f16_f32 v35, v34, v35
	v_cvt_pk_f16_f32 v34, v32, v33
	ds_write_b64 v100, v[34:35] offset:24576
	s_add_u32 s80, s22, 0xc0c00
	s_addc_u32 s81, s90, 0
	global_load_dwordx4 v[88:91], v201, s[80:81] nt
	s_setprio 1
	s_waitcnt lgkmcnt(1)
	v_mfma_f32_16x16x32_f16 v[16:19], v[0:3], v[206:209], v[16:19]
	v_mfma_f32_16x16x32_f16 v[32:35], v[0:3], v[210:213], v[238:241]
	v_mfma_f32_16x16x32_f16 v[170:173], v[0:3], v[214:217], v[170:173]
	v_mfma_f32_16x16x32_f16 v[150:153], v[0:3], v[218:221], v[150:153]
	v_mfma_f32_16x16x32_f16 v[162:165], v[242:245], v[206:209], v[162:165]
	v_mfma_f32_16x16x32_f16 v[174:177], v[242:245], v[210:213], v[174:177]
	v_mfma_f32_16x16x32_f16 v[178:181], v[242:245], v[214:217], v[178:181]
	v_mfma_f32_16x16x32_f16 v[154:157], v[242:245], v[218:221], v[154:157]
	s_setprio 0
	ds_read_b128 v[0:3], v130 offset:45056
	ds_read_b128 v[238:241], v130 offset:47104
	v_cvt_pk_f16_f32 v39, v38, v39
	v_cvt_pk_f16_f32 v38, v36, v37
	ds_write_b64 v100, v[38:39] offset:28672
	s_add_u32 s80, s22, 0xe0c00
	s_addc_u32 s81, s90, 0
	global_load_dwordx4 v[36:39], v201, s[80:81] nt
	s_setprio 1
	s_waitcnt lgkmcnt(1)
	v_mfma_f32_16x16x32_f16 v[20:23], v[0:3], v[206:209], v[20:23]
	v_mfma_f32_16x16x32_f16 v[234:237], v[0:3], v[210:213], v[234:237]
	v_mfma_f32_16x16x32_f16 v[158:161], v[0:3], v[214:217], v[158:161]
	v_mfma_f32_16x16x32_f16 v[166:169], v[0:3], v[218:221], v[166:169]
	v_mfma_f32_16x16x32_f16 v[182:185], v[238:241], v[206:209], v[182:185]
	v_mfma_f32_16x16x32_f16 v[190:193], v[238:241], v[210:213], v[190:193]
	v_mfma_f32_16x16x32_f16 v[202:205], v[238:241], v[214:217], v[202:205]
	v_mfma_f32_16x16x32_f16 v[186:189], v[238:241], v[218:221], v[186:189]
	s_setprio 0
	s_waitcnt vmcnt(4)
	s_waitcnt lgkmcnt(0)
	s_barrier
	ds_read_b128 v[206:209], v131
	ds_read_b128 v[210:213], v131 offset:2048
	ds_read_b128 v[214:217], v131 offset:4096
	ds_read_b128 v[218:221], v131 offset:6144
	ds_read_b128 v[238:241], v129
	ds_read_b128 v[242:245], v129 offset:2048
	s_add_u32 s80, s22, 0xd00
	v_lshl_add_u64 v[92:93], s[48:49], 0, v[196:197]
	s_addc_u32 s81, s90, 0
	s_mov_b32 m0, s0
	v_cvt_pk_f16_f32 v1, v6, v7
	global_load_lds_dwordx4 v[92:93], off
	v_cvt_pk_f16_f32 v0, v4, v5
	ds_write_b64 v100, v[0:1] offset:32768
	global_load_dwordx4 v[0:3], v201, s[80:81] nt
	s_setprio 1
	s_waitcnt lgkmcnt(1)
	v_mfma_f32_16x16x32_f16 v[24:27], v[238:241], v[206:209], v[24:27]
	v_mfma_f32_16x16x32_f16 v[104:107], v[238:241], v[214:217], v[104:107]
	v_mfma_f32_16x16x32_f16 v[108:111], v[242:245], v[206:209], v[108:111]
	v_mfma_f32_16x16x32_f16 v[112:115], v[242:245], v[210:213], v[112:115]
	v_mfma_f32_16x16x32_f16 v[116:119], v[242:245], v[214:217], v[116:119]
	v_mfma_f32_16x16x32_f16 v[230:233], v[238:241], v[210:213], v[230:233]
	v_mfma_f32_16x16x32_f16 v[222:225], v[238:241], v[218:221], v[222:225]
	v_mfma_f32_16x16x32_f16 v[226:229], v[242:245], v[218:221], v[226:229]
	s_setprio 0
	ds_read_b128 v[238:241], v129 offset:4096
	ds_read_b128 v[242:245], v129 offset:6144
	s_mov_b32 m0, s72
	v_lshl_add_u64 v[4:5], v[92:93], 0, s[58:59]
	global_load_lds_dwordx4 v[4:5], off
	v_cvt_pk_f16_f32 v5, v66, v67
	v_cvt_pk_f16_f32 v4, v64, v65
	ds_write_b64 v100, v[4:5] offset:36864
	s_add_u32 s80, s22, 0x20d00
	s_addc_u32 s81, s90, 0
	global_load_dwordx4 v[4:7], v201, s[80:81] nt
	s_setprio 1
	s_waitcnt lgkmcnt(1)
	v_mfma_f32_16x16x32_f16 v[64:67], v[238:241], v[206:209], v[12:15]
	v_mfma_f32_16x16x32_f16 v[28:31], v[238:241], v[210:213], v[28:31]
	v_mfma_f32_16x16x32_f16 v[120:123], v[238:241], v[218:221], v[120:123]
	v_mfma_f32_16x16x32_f16 v[124:127], v[242:245], v[206:209], v[124:127]
	v_mfma_f32_16x16x32_f16 v[146:149], v[242:245], v[214:217], v[146:149]
	v_mfma_f32_16x16x32_f16 v[134:137], v[242:245], v[218:221], v[134:137]
	v_mfma_f32_16x16x32_f16 v[138:141], v[238:241], v[214:217], v[138:141]
	v_mfma_f32_16x16x32_f16 v[142:145], v[242:245], v[210:213], v[142:145]
	s_setprio 0
	ds_read_b128 v[238:241], v129 offset:8192
	ds_read_b128 v[242:245], v129 offset:10240
	s_mov_b32 m0, s71
	v_lshl_add_u64 v[12:13], v[92:93], 0, s[60:61]
	global_load_lds_dwordx4 v[12:13], off
	v_cvt_pk_f16_f32 v13, v42, v43
	v_cvt_pk_f16_f32 v12, v40, v41
	ds_write_b64 v100, v[12:13] offset:40960
	s_add_u32 s80, s22, 0x40d00
	s_addc_u32 s81, s90, 0
	global_load_dwordx4 v[12:15], v201, s[80:81] nt
	s_setprio 1
	s_waitcnt lgkmcnt(1)
	v_mfma_f32_16x16x32_f16 v[40:43], v[238:241], v[206:209], v[16:19]
	v_mfma_f32_16x16x32_f16 v[32:35], v[238:241], v[210:213], v[32:35]
	v_mfma_f32_16x16x32_f16 v[170:173], v[238:241], v[214:217], v[170:173]
	v_mfma_f32_16x16x32_f16 v[150:153], v[238:241], v[218:221], v[150:153]
	v_mfma_f32_16x16x32_f16 v[162:165], v[242:245], v[206:209], v[162:165]
	v_mfma_f32_16x16x32_f16 v[174:177], v[242:245], v[210:213], v[174:177]
	v_mfma_f32_16x16x32_f16 v[178:181], v[242:245], v[214:217], v[178:181]
	v_mfma_f32_16x16x32_f16 v[154:157], v[242:245], v[218:221], v[154:157]
	s_setprio 0
	ds_read_b128 v[238:241], v129 offset:12288
	ds_read_b128 v[242:245], v129 offset:14336
	s_mov_b32 m0, s70
	v_lshl_add_u64 v[16:17], v[92:93], 0, s[62:63]
	global_load_lds_dwordx4 v[16:17], off
	v_cvt_pk_f16_f32 v17, v46, v47
	v_cvt_pk_f16_f32 v16, v44, v45
	ds_write_b64 v100, v[16:17] offset:45056
	s_add_u32 s70, s22, 0x60d00
	s_addc_u32 s71, s90, 0
	global_load_dwordx4 v[16:19], v201, s[70:71] nt
	s_setprio 1
	s_waitcnt lgkmcnt(1)
	v_mfma_f32_16x16x32_f16 v[44:47], v[238:241], v[206:209], v[20:23]
	v_mfma_f32_16x16x32_f16 v[234:237], v[238:241], v[210:213], v[234:237]
	v_mfma_f32_16x16x32_f16 v[158:161], v[238:241], v[214:217], v[158:161]
	v_mfma_f32_16x16x32_f16 v[166:169], v[238:241], v[218:221], v[166:169]
	v_mfma_f32_16x16x32_f16 v[182:185], v[242:245], v[206:209], v[182:185]
	v_mfma_f32_16x16x32_f16 v[190:193], v[242:245], v[210:213], v[190:193]
	v_mfma_f32_16x16x32_f16 v[202:205], v[242:245], v[214:217], v[202:205]
	v_mfma_f32_16x16x32_f16 v[186:189], v[242:245], v[218:221], v[186:189]
	s_setprio 0
	ds_read_b128 v[206:209], v128
	ds_read_b128 v[210:213], v128 offset:2048
	ds_read_b128 v[214:217], v128 offset:4096
	ds_read_b128 v[218:221], v128 offset:6144
	ds_read_b128 v[238:241], v130
	ds_read_b128 v[242:245], v130 offset:2048
	v_cvt_pk_f16_f32 v21, v50, v51
	v_cvt_pk_f16_f32 v20, v48, v49
	ds_write_b64 v100, v[20:21] offset:49152
	s_add_u32 s70, s22, 0x80d00
	s_addc_u32 s71, s90, 0
	global_load_dwordx4 v[20:23], v201, s[70:71] nt
	s_setprio 1
	s_waitcnt lgkmcnt(1)
	v_mfma_f32_16x16x32_f16 v[48:51], v[238:241], v[206:209], v[24:27]
	v_mfma_f32_16x16x32_f16 v[104:107], v[238:241], v[214:217], v[104:107]
	v_mfma_f32_16x16x32_f16 v[108:111], v[242:245], v[206:209], v[108:111]
	v_mfma_f32_16x16x32_f16 v[112:115], v[242:245], v[210:213], v[112:115]
	v_mfma_f32_16x16x32_f16 v[116:119], v[242:245], v[214:217], v[116:119]
	v_mfma_f32_16x16x32_f16 v[230:233], v[238:241], v[210:213], v[230:233]
	v_mfma_f32_16x16x32_f16 v[222:225], v[238:241], v[218:221], v[222:225]
	v_mfma_f32_16x16x32_f16 v[226:229], v[242:245], v[218:221], v[226:229]
	s_setprio 0
	ds_read_b128 v[238:241], v130 offset:4096
	ds_read_b128 v[242:245], v130 offset:6144
	v_cvt_pk_f16_f32 v25, v54, v55
	v_cvt_pk_f16_f32 v24, v52, v53
	ds_write_b64 v100, v[24:25] offset:53248
	s_add_u32 s70, s22, 0xa0d00
	s_addc_u32 s71, s90, 0
	global_load_dwordx4 v[24:27], v201, s[70:71] nt
	s_setprio 1
	s_waitcnt lgkmcnt(1)
	v_mfma_f32_16x16x32_f16 v[52:55], v[238:241], v[206:209], v[64:67]
	v_mfma_f32_16x16x32_f16 v[64:67], v[238:241], v[210:213], v[28:31]
	v_mfma_f32_16x16x32_f16 v[120:123], v[238:241], v[218:221], v[120:123]
	v_mfma_f32_16x16x32_f16 v[124:127], v[242:245], v[206:209], v[124:127]
	v_mfma_f32_16x16x32_f16 v[146:149], v[242:245], v[214:217], v[146:149]
	v_mfma_f32_16x16x32_f16 v[134:137], v[242:245], v[218:221], v[134:137]
	v_mfma_f32_16x16x32_f16 v[138:141], v[238:241], v[214:217], v[138:141]
	v_mfma_f32_16x16x32_f16 v[142:145], v[242:245], v[210:213], v[142:145]
	s_setprio 0
	ds_read_b128 v[238:241], v130 offset:8192
	ds_read_b128 v[242:245], v130 offset:10240
	v_cvt_pk_f16_f32 v29, v58, v59
	v_cvt_pk_f16_f32 v28, v56, v57
	ds_write_b64 v100, v[28:29] offset:57344
	s_add_u32 s70, s22, 0xc0d00
	s_addc_u32 s71, s90, 0
	global_load_dwordx4 v[28:31], v201, s[70:71] nt
	s_setprio 1
	s_waitcnt lgkmcnt(1)
	v_mfma_f32_16x16x32_f16 v[56:59], v[238:241], v[206:209], v[40:43]
	v_mfma_f32_16x16x32_f16 v[246:249], v[238:241], v[210:213], v[32:35]
	v_mfma_f32_16x16x32_f16 v[170:173], v[238:241], v[214:217], v[170:173]
	v_mfma_f32_16x16x32_f16 v[150:153], v[238:241], v[218:221], v[150:153]
	v_mfma_f32_16x16x32_f16 v[162:165], v[242:245], v[206:209], v[162:165]
	v_mfma_f32_16x16x32_f16 v[174:177], v[242:245], v[210:213], v[174:177]
	v_mfma_f32_16x16x32_f16 v[178:181], v[242:245], v[214:217], v[178:181]
	v_mfma_f32_16x16x32_f16 v[154:157], v[242:245], v[218:221], v[154:157]
	s_setprio 0
	ds_read_b128 v[40:43], v130 offset:12288
	ds_read_b128 v[238:241], v130 offset:14336
	v_cvt_pk_f16_f32 v33, v62, v63
	v_cvt_pk_f16_f32 v32, v60, v61
	ds_write_b64 v100, v[32:33] offset:61440
	s_add_u32 s70, s22, 0xe0d00
	s_addc_u32 s71, s90, 0
	global_load_dwordx4 v[32:35], v201, s[70:71] nt
	s_setprio 1
	s_waitcnt lgkmcnt(1)
	v_mfma_f32_16x16x32_f16 v[60:63], v[40:43], v[206:209], v[44:47]
	v_mfma_f32_16x16x32_f16 v[234:237], v[40:43], v[210:213], v[234:237]
	v_mfma_f32_16x16x32_f16 v[158:161], v[40:43], v[214:217], v[158:161]
	v_mfma_f32_16x16x32_f16 v[166:169], v[40:43], v[218:221], v[166:169]
	v_mfma_f32_16x16x32_f16 v[182:185], v[238:241], v[206:209], v[182:185]
	v_mfma_f32_16x16x32_f16 v[190:193], v[238:241], v[210:213], v[190:193]
	v_mfma_f32_16x16x32_f16 v[202:205], v[238:241], v[214:217], v[202:205]
	v_mfma_f32_16x16x32_f16 v[186:189], v[238:241], v[218:221], v[186:189]
	s_setprio 0
	s_waitcnt vmcnt(4)
	s_waitcnt lgkmcnt(0)
	s_barrier
	ds_read_b128 v[206:209], v131 offset:32768
	ds_read_b128 v[210:213], v131 offset:34816
	ds_read_b128 v[214:217], v131 offset:36864
	ds_read_b128 v[218:221], v131 offset:38912
	ds_read_b128 v[40:43], v129 offset:32768
	ds_read_b128 v[44:47], v129 offset:34816
	s_add_u32 s70, s22, 0xe00
	v_lshl_add_u64 v[92:93], s[50:51], 0, v[196:197]
	s_addc_u32 s71, s90, 0
	s_mov_b32 m0, s1
	v_cvt_pk_f16_f32 v11, v10, v11
	global_load_lds_dwordx4 v[92:93], off
	v_cvt_pk_f16_f32 v10, v8, v9
	ds_write_b64 v100, v[10:11]
	global_load_dwordx4 v[8:11], v201, s[70:71] nt
	s_setprio 1
	s_waitcnt lgkmcnt(1)
	v_mfma_f32_16x16x32_f16 v[104:107], v[40:43], v[214:217], v[104:107]
	v_mfma_f32_16x16x32_f16 v[108:111], v[44:47], v[206:209], v[108:111]
	v_mfma_f32_16x16x32_f16 v[112:115], v[44:47], v[210:213], v[112:115]
	v_mfma_f32_16x16x32_f16 v[116:119], v[44:47], v[214:217], v[116:119]
	v_mfma_f32_16x16x32_f16 v[238:241], v[40:43], v[206:209], v[48:51]
	v_mfma_f32_16x16x32_f16 v[230:233], v[40:43], v[210:213], v[230:233]
	v_mfma_f32_16x16x32_f16 v[222:225], v[40:43], v[218:221], v[222:225]
	v_mfma_f32_16x16x32_f16 v[226:229], v[44:47], v[218:221], v[226:229]
	s_setprio 0
	ds_read_b128 v[44:47], v129 offset:36864
	ds_read_b128 v[48:51], v129 offset:38912
	s_mov_b32 m0, s92
	v_lshl_add_u64 v[40:41], v[92:93], 0, s[58:59]
	global_load_lds_dwordx4 v[40:41], off
	v_cvt_pk_f16_f32 v41, v70, v71
	v_cvt_pk_f16_f32 v40, v68, v69
	ds_write_b64 v100, v[40:41] offset:4096
	s_add_u32 s0, s22, 0x20e00
	s_addc_u32 s1, s90, 0
	global_load_dwordx4 v[40:43], v201, s[0:1] nt
	s_setprio 1
	s_waitcnt lgkmcnt(1)
	v_mfma_f32_16x16x32_f16 v[68:71], v[44:47], v[206:209], v[52:55]
	v_mfma_f32_16x16x32_f16 v[64:67], v[44:47], v[210:213], v[64:67]
	v_mfma_f32_16x16x32_f16 v[120:123], v[44:47], v[218:221], v[120:123]
	v_mfma_f32_16x16x32_f16 v[124:127], v[48:51], v[206:209], v[124:127]
	v_mfma_f32_16x16x32_f16 v[146:149], v[48:51], v[214:217], v[146:149]
	v_mfma_f32_16x16x32_f16 v[134:137], v[48:51], v[218:221], v[134:137]
	v_mfma_f32_16x16x32_f16 v[138:141], v[44:47], v[214:217], v[138:141]
	v_mfma_f32_16x16x32_f16 v[142:145], v[48:51], v[210:213], v[142:145]
	s_setprio 0
	ds_read_b128 v[48:51], v129 offset:40960
	ds_read_b128 v[52:55], v129 offset:43008
	s_mov_b32 m0, s91
	v_lshl_add_u64 v[44:45], v[92:93], 0, s[60:61]
	global_load_lds_dwordx4 v[44:45], off
	v_cvt_pk_f16_f32 v45, v74, v75
	v_cvt_pk_f16_f32 v44, v72, v73
	ds_write_b64 v100, v[44:45] offset:8192
	s_add_u32 s0, s22, 0x40e00
	s_addc_u32 s1, s90, 0
	global_load_dwordx4 v[44:47], v201, s[0:1] nt
	s_setprio 1
	s_waitcnt lgkmcnt(1)
	v_mfma_f32_16x16x32_f16 v[72:75], v[48:51], v[206:209], v[56:59]
	v_mfma_f32_16x16x32_f16 v[242:245], v[48:51], v[210:213], v[246:249]
	v_mfma_f32_16x16x32_f16 v[170:173], v[48:51], v[214:217], v[170:173]
	v_mfma_f32_16x16x32_f16 v[150:153], v[48:51], v[218:221], v[150:153]
	v_mfma_f32_16x16x32_f16 v[162:165], v[52:55], v[206:209], v[162:165]
	v_mfma_f32_16x16x32_f16 v[174:177], v[52:55], v[210:213], v[174:177]
	v_mfma_f32_16x16x32_f16 v[178:181], v[52:55], v[214:217], v[178:181]
	v_mfma_f32_16x16x32_f16 v[154:157], v[52:55], v[218:221], v[154:157]
	s_setprio 0
	ds_read_b128 v[52:55], v129 offset:45056
	ds_read_b128 v[56:59], v129 offset:47104
	s_mov_b32 m0, s73
	v_lshl_add_u64 v[48:49], v[92:93], 0, s[62:63]
	global_load_lds_dwordx4 v[48:49], off
	v_cvt_pk_f16_f32 v49, v78, v79
	v_cvt_pk_f16_f32 v48, v76, v77
	ds_write_b64 v100, v[48:49] offset:12288
	s_add_u32 s0, s22, 0x60e00
	s_addc_u32 s1, s90, 0
	global_load_dwordx4 v[48:51], v201, s[0:1] nt
	s_setprio 1
	s_waitcnt lgkmcnt(1)
	v_mfma_f32_16x16x32_f16 v[76:79], v[52:55], v[206:209], v[60:63]
	v_mfma_f32_16x16x32_f16 v[234:237], v[52:55], v[210:213], v[234:237]
	v_mfma_f32_16x16x32_f16 v[158:161], v[52:55], v[214:217], v[158:161]
	v_mfma_f32_16x16x32_f16 v[166:169], v[52:55], v[218:221], v[166:169]
	v_mfma_f32_16x16x32_f16 v[182:185], v[56:59], v[206:209], v[182:185]
	v_mfma_f32_16x16x32_f16 v[190:193], v[56:59], v[210:213], v[190:193]
	v_mfma_f32_16x16x32_f16 v[202:205], v[56:59], v[214:217], v[202:205]
	v_mfma_f32_16x16x32_f16 v[186:189], v[56:59], v[218:221], v[186:189]
	s_setprio 0
	ds_read_b128 v[206:209], v128 offset:32768
	ds_read_b128 v[210:213], v128 offset:34816
	ds_read_b128 v[214:217], v128 offset:36864
	ds_read_b128 v[218:221], v128 offset:38912
	ds_read_b128 v[56:59], v130 offset:32768
	ds_read_b128 v[60:63], v130 offset:34816
	v_cvt_pk_f16_f32 v53, v82, v83
	v_cvt_pk_f16_f32 v52, v80, v81
	ds_write_b64 v100, v[52:53] offset:16384
	s_add_u32 s0, s22, 0x80e00
	s_addc_u32 s1, s90, 0
	global_load_dwordx4 v[52:55], v201, s[0:1] nt
	s_setprio 1
	s_waitcnt lgkmcnt(1)
	v_mfma_f32_16x16x32_f16 v[80:83], v[56:59], v[206:209], v[238:241]
	v_mfma_f32_16x16x32_f16 v[104:107], v[56:59], v[214:217], v[104:107]
	v_mfma_f32_16x16x32_f16 v[108:111], v[60:63], v[206:209], v[108:111]
	v_mfma_f32_16x16x32_f16 v[112:115], v[60:63], v[210:213], v[112:115]
	v_mfma_f32_16x16x32_f16 v[116:119], v[60:63], v[214:217], v[116:119]
	v_mfma_f32_16x16x32_f16 v[230:233], v[56:59], v[210:213], v[230:233]
	v_mfma_f32_16x16x32_f16 v[222:225], v[56:59], v[218:221], v[222:225]
	v_mfma_f32_16x16x32_f16 v[226:229], v[60:63], v[218:221], v[226:229]
	s_setprio 0
	ds_read_b128 v[60:63], v130 offset:36864
	ds_read_b128 v[238:241], v130 offset:38912
	v_cvt_pk_f16_f32 v57, v86, v87
	v_cvt_pk_f16_f32 v56, v84, v85
	ds_write_b64 v100, v[56:57] offset:20480
	s_add_u32 s0, s22, 0xa0e00
	s_addc_u32 s1, s90, 0
	global_load_dwordx4 v[56:59], v201, s[0:1] nt
	s_setprio 1
	s_waitcnt lgkmcnt(1)
	v_mfma_f32_16x16x32_f16 v[68:71], v[60:63], v[206:209], v[68:71]
	v_mfma_f32_16x16x32_f16 v[64:67], v[60:63], v[210:213], v[64:67]
	v_mfma_f32_16x16x32_f16 v[84:87], v[60:63], v[214:217], v[138:141]
	v_mfma_f32_16x16x32_f16 v[120:123], v[60:63], v[218:221], v[120:123]
	v_mfma_f32_16x16x32_f16 v[124:127], v[238:241], v[206:209], v[124:127]
	v_mfma_f32_16x16x32_f16 v[134:137], v[238:241], v[218:221], v[134:137]
	v_mfma_f32_16x16x32_f16 v[138:141], v[238:241], v[210:213], v[142:145]
	v_mfma_f32_16x16x32_f16 v[142:145], v[238:241], v[214:217], v[146:149]
	s_setprio 0
	s_nop 1
	ds_read_b128 v[146:149], v130 offset:40960
	ds_read_b128 v[238:241], v130 offset:43008
	v_cvt_pk_f16_f32 v61, v90, v91
	v_cvt_pk_f16_f32 v60, v88, v89
	ds_write_b64 v100, v[60:61] offset:24576
	s_add_u32 s0, s22, 0xc0e00
	s_addc_u32 s1, s90, 0
	global_load_dwordx4 v[60:63], v201, s[0:1] nt
	s_setprio 1
	s_waitcnt lgkmcnt(1)
	v_mfma_f32_16x16x32_f16 v[72:75], v[146:149], v[206:209], v[72:75]
	v_mfma_f32_16x16x32_f16 v[88:91], v[146:149], v[210:213], v[242:245]
	v_mfma_f32_16x16x32_f16 v[170:173], v[146:149], v[214:217], v[170:173]
	v_mfma_f32_16x16x32_f16 v[146:149], v[146:149], v[218:221], v[150:153]
	v_mfma_f32_16x16x32_f16 v[150:153], v[238:241], v[206:209], v[162:165]
	v_mfma_f32_16x16x32_f16 v[162:165], v[238:241], v[210:213], v[174:177]
	v_mfma_f32_16x16x32_f16 v[174:177], v[238:241], v[214:217], v[178:181]
	v_mfma_f32_16x16x32_f16 v[154:157], v[238:241], v[218:221], v[154:157]
	s_setprio 0
	s_nop 0
	ds_read_b128 v[178:181], v130 offset:45056
	ds_read_b128 v[238:241], v130 offset:47104
	v_cvt_pk_f16_f32 v39, v38, v39
	v_cvt_pk_f16_f32 v38, v36, v37
	ds_write_b64 v100, v[38:39] offset:28672
	s_add_u32 s0, s22, 0xe0e00
	s_addc_u32 s1, s90, 0
	global_load_dwordx4 v[36:39], v201, s[0:1] nt
	s_setprio 1
	s_waitcnt lgkmcnt(1)
	v_mfma_f32_16x16x32_f16 v[76:79], v[178:181], v[206:209], v[76:79]
	v_mfma_f32_16x16x32_f16 v[234:237], v[178:181], v[210:213], v[234:237]
	v_mfma_f32_16x16x32_f16 v[158:161], v[178:181], v[214:217], v[158:161]
	v_mfma_f32_16x16x32_f16 v[166:169], v[178:181], v[218:221], v[166:169]
	v_mfma_f32_16x16x32_f16 v[178:181], v[238:241], v[206:209], v[182:185]
	v_mfma_f32_16x16x32_f16 v[182:185], v[238:241], v[210:213], v[190:193]
	v_mfma_f32_16x16x32_f16 v[190:193], v[238:241], v[214:217], v[202:205]
	v_mfma_f32_16x16x32_f16 v[186:189], v[238:241], v[218:221], v[186:189]
	s_setprio 0
	s_waitcnt vmcnt(4)
	s_waitcnt lgkmcnt(0)
	s_barrier
	ds_read_b128 v[202:205], v131
	ds_read_b128 v[206:209], v131 offset:2048
	ds_read_b128 v[210:213], v131 offset:4096
	ds_read_b128 v[214:217], v131 offset:6144
	ds_read_b128 v[218:221], v129
	ds_read_b128 v[238:241], v129 offset:2048
	s_add_u32 s70, s22, 0xf00
	v_lshl_add_u64 v[92:93], s[52:53], 0, v[196:197]
	s_addc_u32 s71, s90, 0
	v_readfirstlane_b32 s0, v95
	s_mov_b32 m0, s0
	v_cvt_pk_f16_f32 v3, v2, v3
	global_load_lds_dwordx4 v[92:93], off
	v_cvt_pk_f16_f32 v2, v0, v1
	ds_write_b64 v100, v[2:3] offset:32768
	global_load_dwordx4 v[0:3], v201, s[70:71] nt
	s_setprio 1
	s_waitcnt lgkmcnt(1)
	v_mfma_f32_16x16x32_f16 v[80:83], v[218:221], v[202:205], v[80:83]
	v_mfma_f32_16x16x32_f16 v[104:107], v[218:221], v[210:213], v[104:107]
	v_mfma_f32_16x16x32_f16 v[108:111], v[238:241], v[202:205], v[108:111]
	v_mfma_f32_16x16x32_f16 v[112:115], v[238:241], v[206:209], v[112:115]
	v_mfma_f32_16x16x32_f16 v[116:119], v[238:241], v[210:213], v[116:119]
	v_mfma_f32_16x16x32_f16 v[230:233], v[218:221], v[206:209], v[230:233]
	v_mfma_f32_16x16x32_f16 v[218:221], v[218:221], v[214:217], v[222:225]
	v_mfma_f32_16x16x32_f16 v[222:225], v[238:241], v[214:217], v[226:229]
	s_setprio 0
	s_nop 1
	ds_read_b128 v[226:229], v129 offset:4096
	ds_read_b128 v[238:241], v129 offset:6144
	v_readfirstlane_b32 s1, v96
	v_lshl_add_u64 v[198:199], v[92:93], 0, s[58:59]
	s_mov_b32 m0, s1
	v_cvt_pk_f16_f32 v7, v6, v7
	global_load_lds_dwordx4 v[198:199], off
	v_cvt_pk_f16_f32 v6, v4, v5
	ds_write_b64 v100, v[6:7] offset:36864
	s_add_u32 s70, s22, 0x20f00
	s_addc_u32 s71, s90, 0
	global_load_dwordx4 v[4:7], v201, s[70:71] nt
	s_setprio 1
	s_waitcnt lgkmcnt(1)
	v_mfma_f32_16x16x32_f16 v[68:71], v[226:229], v[202:205], v[68:71]
	v_mfma_f32_16x16x32_f16 v[64:67], v[226:229], v[206:209], v[64:67]
	v_mfma_f32_16x16x32_f16 v[84:87], v[226:229], v[210:213], v[84:87]
	v_mfma_f32_16x16x32_f16 v[120:123], v[226:229], v[214:217], v[120:123]
	v_mfma_f32_16x16x32_f16 v[124:127], v[238:241], v[202:205], v[124:127]
	v_mfma_f32_16x16x32_f16 v[134:137], v[238:241], v[214:217], v[134:137]
	v_mfma_f32_16x16x32_f16 v[138:141], v[238:241], v[206:209], v[138:141]
	v_mfma_f32_16x16x32_f16 v[142:145], v[238:241], v[210:213], v[142:145]
	s_setprio 0
	ds_read_b128 v[226:229], v129 offset:8192
	ds_read_b128 v[238:241], v129 offset:10240
	v_readfirstlane_b32 s70, v97
	v_lshl_add_u64 v[198:199], v[92:93], 0, s[60:61]
	s_mov_b32 m0, s70
	v_cvt_pk_f16_f32 v15, v14, v15
	global_load_lds_dwordx4 v[198:199], off
	v_cvt_pk_f16_f32 v14, v12, v13
	ds_write_b64 v100, v[14:15] offset:40960
	s_add_u32 s72, s22, 0x40f00
	s_addc_u32 s73, s90, 0
	global_load_dwordx4 v[12:15], v201, s[72:73] nt
	s_setprio 1
	s_waitcnt lgkmcnt(1)
	v_mfma_f32_16x16x32_f16 v[72:75], v[226:229], v[202:205], v[72:75]
	v_mfma_f32_16x16x32_f16 v[88:91], v[226:229], v[206:209], v[88:91]
	v_mfma_f32_16x16x32_f16 v[146:149], v[226:229], v[214:217], v[146:149]
	v_mfma_f32_16x16x32_f16 v[170:173], v[226:229], v[210:213], v[170:173]
	v_mfma_f32_16x16x32_f16 v[150:153], v[238:241], v[202:205], v[150:153]
	v_mfma_f32_16x16x32_f16 v[162:165], v[238:241], v[206:209], v[162:165]
	v_mfma_f32_16x16x32_f16 v[174:177], v[238:241], v[210:213], v[174:177]
	v_mfma_f32_16x16x32_f16 v[154:157], v[238:241], v[214:217], v[154:157]
	s_setprio 0
	ds_read_b128 v[226:229], v129 offset:12288
	ds_read_b128 v[238:241], v129 offset:14336
	v_readfirstlane_b32 s71, v98
	v_lshl_add_u64 v[92:93], v[92:93], 0, s[62:63]
	s_mov_b32 m0, s71
	v_cvt_pk_f16_f32 v19, v18, v19
	global_load_lds_dwordx4 v[92:93], off
	v_cvt_pk_f16_f32 v18, v16, v17
	ds_write_b64 v100, v[18:19] offset:45056
	s_add_u32 s72, s22, 0x60f00
	s_addc_u32 s73, s90, 0
	global_load_dwordx4 v[16:19], v201, s[72:73] nt
	s_setprio 1
	s_waitcnt lgkmcnt(1)
	v_mfma_f32_16x16x32_f16 v[76:79], v[226:229], v[202:205], v[76:79]
	v_mfma_f32_16x16x32_f16 v[234:237], v[226:229], v[206:209], v[234:237]
	v_mfma_f32_16x16x32_f16 v[158:161], v[226:229], v[210:213], v[158:161]
	v_mfma_f32_16x16x32_f16 v[166:169], v[226:229], v[214:217], v[166:169]
	v_mfma_f32_16x16x32_f16 v[178:181], v[238:241], v[202:205], v[178:181]
	v_mfma_f32_16x16x32_f16 v[182:185], v[238:241], v[206:209], v[182:185]
	v_mfma_f32_16x16x32_f16 v[190:193], v[238:241], v[210:213], v[190:193]
	v_mfma_f32_16x16x32_f16 v[186:189], v[238:241], v[214:217], v[186:189]
	s_setprio 0
	ds_read_b128 v[202:205], v128
	ds_read_b128 v[206:209], v128 offset:2048
	ds_read_b128 v[210:213], v128 offset:4096
	ds_read_b128 v[214:217], v128 offset:6144
	ds_read_b128 v[226:229], v130
	ds_read_b128 v[238:241], v130 offset:2048
	v_cvt_pk_f16_f32 v23, v22, v23
	v_cvt_pk_f16_f32 v22, v20, v21
	ds_write_b64 v100, v[22:23] offset:49152
	s_add_u32 s72, s22, 0x80f00
	s_addc_u32 s73, s90, 0
	global_load_dwordx4 v[20:23], v201, s[72:73] nt
	s_setprio 1
	s_waitcnt lgkmcnt(1)
	v_mfma_f32_16x16x32_f16 v[80:83], v[226:229], v[202:205], v[80:83]
	v_mfma_f32_16x16x32_f16 v[104:107], v[226:229], v[210:213], v[104:107]
	v_mfma_f32_16x16x32_f16 v[108:111], v[238:241], v[202:205], v[108:111]
	v_mfma_f32_16x16x32_f16 v[112:115], v[238:241], v[206:209], v[112:115]
	v_mfma_f32_16x16x32_f16 v[116:119], v[238:241], v[210:213], v[116:119]
	v_mfma_f32_16x16x32_f16 v[230:233], v[226:229], v[206:209], v[230:233]
	v_mfma_f32_16x16x32_f16 v[218:221], v[226:229], v[214:217], v[218:221]
	v_mfma_f32_16x16x32_f16 v[222:225], v[238:241], v[214:217], v[222:225]
	s_setprio 0
	ds_read_b128 v[226:229], v130 offset:4096
	ds_read_b128 v[238:241], v130 offset:6144
	v_cvt_pk_f16_f32 v27, v26, v27
	v_cvt_pk_f16_f32 v26, v24, v25
	ds_write_b64 v100, v[26:27] offset:53248
	s_add_u32 s72, s22, 0xa0f00
	s_addc_u32 s73, s90, 0
	global_load_dwordx4 v[24:27], v201, s[72:73] nt
	s_setprio 1
	s_waitcnt lgkmcnt(1)
	v_mfma_f32_16x16x32_f16 v[68:71], v[226:229], v[202:205], v[68:71]
	v_mfma_f32_16x16x32_f16 v[64:67], v[226:229], v[206:209], v[64:67]
	v_mfma_f32_16x16x32_f16 v[84:87], v[226:229], v[210:213], v[84:87]
	v_mfma_f32_16x16x32_f16 v[120:123], v[226:229], v[214:217], v[120:123]
	v_mfma_f32_16x16x32_f16 v[124:127], v[238:241], v[202:205], v[124:127]
	v_mfma_f32_16x16x32_f16 v[134:137], v[238:241], v[214:217], v[134:137]
	v_mfma_f32_16x16x32_f16 v[138:141], v[238:241], v[206:209], v[138:141]
	v_mfma_f32_16x16x32_f16 v[142:145], v[238:241], v[210:213], v[142:145]
	s_setprio 0
	ds_read_b128 v[226:229], v130 offset:8192
	ds_read_b128 v[238:241], v130 offset:10240
	v_cvt_pk_f16_f32 v31, v30, v31
	v_cvt_pk_f16_f32 v30, v28, v29
	ds_write_b64 v100, v[30:31] offset:57344
	s_add_u32 s72, s22, 0xc0f00
	s_addc_u32 s73, s90, 0
	global_load_dwordx4 v[28:31], v201, s[72:73] nt
	s_setprio 1
	s_waitcnt lgkmcnt(1)
	v_mfma_f32_16x16x32_f16 v[72:75], v[226:229], v[202:205], v[72:75]
	v_mfma_f32_16x16x32_f16 v[88:91], v[226:229], v[206:209], v[88:91]
	v_mfma_f32_16x16x32_f16 v[146:149], v[226:229], v[214:217], v[146:149]
	v_mfma_f32_16x16x32_f16 v[170:173], v[226:229], v[210:213], v[170:173]
	v_mfma_f32_16x16x32_f16 v[150:153], v[238:241], v[202:205], v[150:153]
	v_mfma_f32_16x16x32_f16 v[162:165], v[238:241], v[206:209], v[162:165]
	v_mfma_f32_16x16x32_f16 v[174:177], v[238:241], v[210:213], v[174:177]
	v_mfma_f32_16x16x32_f16 v[154:157], v[238:241], v[214:217], v[154:157]
	s_setprio 0
	ds_read_b128 v[226:229], v130 offset:12288
	ds_read_b128 v[238:241], v130 offset:14336
	v_cvt_pk_f16_f32 v35, v34, v35
	v_cvt_pk_f16_f32 v34, v32, v33
	ds_write_b64 v100, v[34:35] offset:61440
	s_add_u32 s72, s22, 0xe0f00
	s_addc_u32 s73, s90, 0
	global_load_dwordx4 v[32:35], v201, s[72:73] nt
	s_setprio 1
	s_waitcnt lgkmcnt(1)
	v_mfma_f32_16x16x32_f16 v[76:79], v[226:229], v[202:205], v[76:79]
	v_mfma_f32_16x16x32_f16 v[234:237], v[226:229], v[206:209], v[234:237]
	v_mfma_f32_16x16x32_f16 v[158:161], v[226:229], v[210:213], v[158:161]
	v_mfma_f32_16x16x32_f16 v[166:169], v[226:229], v[214:217], v[166:169]
	v_mfma_f32_16x16x32_f16 v[178:181], v[238:241], v[202:205], v[178:181]
	v_mfma_f32_16x16x32_f16 v[182:185], v[238:241], v[206:209], v[182:185]
	v_mfma_f32_16x16x32_f16 v[190:193], v[238:241], v[210:213], v[190:193]
	v_mfma_f32_16x16x32_f16 v[186:189], v[238:241], v[214:217], v[186:189]
	s_setprio 0
	s_waitcnt vmcnt(4)
	s_waitcnt lgkmcnt(0)
	s_barrier
	ds_read_b128 v[202:205], v131 offset:32768
	ds_read_b128 v[206:209], v131 offset:34816
	ds_read_b128 v[210:213], v131 offset:36864
	ds_read_b128 v[214:217], v131 offset:38912
	ds_read_b128 v[226:229], v129 offset:32768
	ds_read_b128 v[238:241], v129 offset:34816
	v_lshl_add_u64 v[198:199], s[54:55], 0, v[196:197]
	v_readfirstlane_b32 s64, v94
	s_mov_b32 m0, s64
	v_cvt_pk_f16_f32 v11, v10, v11
	global_load_lds_dwordx4 v[198:199], off
	v_cvt_pk_f16_f32 v10, v8, v9
	ds_write_b64 v100, v[10:11]
	s_setprio 1
	s_waitcnt lgkmcnt(1)
	v_mfma_f32_16x16x32_f16 v[8:11], v[226:229], v[202:205], v[80:83]
	v_mfma_f32_16x16x32_f16 v[80:83], v[226:229], v[206:209], v[230:233]
	v_mfma_f32_16x16x32_f16 v[92:95], v[226:229], v[210:213], v[104:107]
	v_mfma_f32_16x16x32_f16 v[104:107], v[226:229], v[214:217], v[218:221]
	v_mfma_f32_16x16x32_f16 v[108:111], v[238:241], v[202:205], v[108:111]
	v_mfma_f32_16x16x32_f16 v[112:115], v[238:241], v[206:209], v[112:115]
	v_mfma_f32_16x16x32_f16 v[116:119], v[238:241], v[210:213], v[116:119]
	v_mfma_f32_16x16x32_f16 v[218:221], v[238:241], v[214:217], v[222:225]
	s_setprio 0
	s_nop 1
	ds_read_b128 v[222:225], v129 offset:36864
	ds_read_b128 v[226:229], v129 offset:38912
	v_readfirstlane_b32 s64, v99
	v_lshl_add_u64 v[96:97], v[198:199], 0, s[58:59]
	s_mov_b32 m0, s64
	v_cvt_pk_f16_f32 v43, v42, v43
	global_load_lds_dwordx4 v[96:97], off
	v_cvt_pk_f16_f32 v42, v40, v41
	ds_write_b64 v100, v[42:43] offset:4096
	s_setprio 1
	s_waitcnt lgkmcnt(1)
	v_mfma_f32_16x16x32_f16 v[40:43], v[222:225], v[202:205], v[68:71]
	v_mfma_f32_16x16x32_f16 v[64:67], v[222:225], v[206:209], v[64:67]
	v_mfma_f32_16x16x32_f16 v[68:71], v[222:225], v[210:213], v[84:87]
	v_mfma_f32_16x16x32_f16 v[84:87], v[222:225], v[214:217], v[120:123]
	v_mfma_f32_16x16x32_f16 v[96:99], v[226:229], v[202:205], v[124:127]
	v_mfma_f32_16x16x32_f16 v[120:123], v[226:229], v[206:209], v[138:141]
	v_mfma_f32_16x16x32_f16 v[124:127], v[226:229], v[210:213], v[142:145]
	v_mfma_f32_16x16x32_f16 v[134:137], v[226:229], v[214:217], v[134:137]
	s_setprio 0
	ds_read_b128 v[138:141], v129 offset:40960
	ds_read_b128 v[142:145], v129 offset:43008
	v_readfirstlane_b32 s64, v101
	v_lshl_add_u64 v[222:223], v[198:199], 0, s[60:61]
	s_mov_b32 m0, s64
	v_cvt_pk_f16_f32 v47, v46, v47
	global_load_lds_dwordx4 v[222:223], off
	v_cvt_pk_f16_f32 v46, v44, v45
	ds_write_b64 v100, v[46:47] offset:8192
	s_setprio 1
	s_waitcnt lgkmcnt(1)
	v_mfma_f32_16x16x32_f16 v[44:47], v[138:141], v[202:205], v[72:75]
	v_mfma_f32_16x16x32_f16 v[72:75], v[138:141], v[206:209], v[88:91]
	v_mfma_f32_16x16x32_f16 v[88:91], v[138:141], v[210:213], v[170:173]
	v_mfma_f32_16x16x32_f16 v[138:141], v[138:141], v[214:217], v[146:149]
	v_mfma_f32_16x16x32_f16 v[146:149], v[142:145], v[202:205], v[150:153]
	v_mfma_f32_16x16x32_f16 v[150:153], v[142:145], v[206:209], v[162:165]
	v_mfma_f32_16x16x32_f16 v[162:165], v[142:145], v[210:213], v[174:177]
	v_mfma_f32_16x16x32_f16 v[142:145], v[142:145], v[214:217], v[154:157]
	s_setprio 0
	s_nop 1
	ds_read_b128 v[154:157], v129 offset:45056
	ds_read_b128 v[170:173], v129 offset:47104
	v_readfirstlane_b32 s64, v102
	v_lshl_add_u64 v[174:175], v[198:199], 0, s[62:63]
	s_mov_b32 m0, s64
	v_cvt_pk_f16_f32 v51, v50, v51
	global_load_lds_dwordx4 v[174:175], off
	v_cvt_pk_f16_f32 v50, v48, v49
	ds_write_b64 v100, v[50:51] offset:12288
	s_setprio 1
	s_waitcnt lgkmcnt(1)
	v_mfma_f32_16x16x32_f16 v[48:51], v[154:157], v[202:205], v[76:79]
	v_mfma_f32_16x16x32_f16 v[76:79], v[154:157], v[206:209], v[234:237]
	v_mfma_f32_16x16x32_f16 v[158:161], v[154:157], v[210:213], v[158:161]
	v_mfma_f32_16x16x32_f16 v[154:157], v[154:157], v[214:217], v[166:169]
	v_mfma_f32_16x16x32_f16 v[166:169], v[170:173], v[202:205], v[178:181]
	v_mfma_f32_16x16x32_f16 v[174:177], v[170:173], v[206:209], v[182:185]
	v_mfma_f32_16x16x32_f16 v[178:181], v[170:173], v[210:213], v[190:193]
	v_mfma_f32_16x16x32_f16 v[170:173], v[170:173], v[214:217], v[186:189]
	s_setprio 0
	ds_read_b128 v[182:185], v128 offset:32768
	s_nop 0
	ds_read_b128 v[186:189], v128 offset:34816
	ds_read_b128 v[190:193], v128 offset:36864
	ds_read_b128 v[202:205], v128 offset:38912
	ds_read_b128 v[206:209], v130 offset:32768
	ds_read_b128 v[210:213], v130 offset:34816
	v_cvt_pk_f16_f32 v55, v54, v55
	v_cvt_pk_f16_f32 v54, v52, v53
	ds_write_b64 v100, v[54:55] offset:16384
	s_setprio 1
	s_waitcnt lgkmcnt(1)
	v_mfma_f32_16x16x32_f16 v[8:11], v[206:209], v[182:185], v[8:11]
	v_mfma_f32_16x16x32_f16 v[52:55], v[206:209], v[186:189], v[80:83]
	v_mfma_f32_16x16x32_f16 v[80:83], v[206:209], v[190:193], v[92:95]
	v_mfma_f32_16x16x32_f16 v[92:95], v[206:209], v[202:205], v[104:107]
	v_mfma_f32_16x16x32_f16 v[102:105], v[210:213], v[182:185], v[108:111]
	v_mfma_f32_16x16x32_f16 v[106:109], v[210:213], v[186:189], v[112:115]
	v_mfma_f32_16x16x32_f16 v[110:113], v[210:213], v[190:193], v[116:119]
	v_mfma_f32_16x16x32_f16 v[114:117], v[210:213], v[202:205], v[218:221]
	s_setprio 0
	ds_read_b128 v[206:209], v130 offset:36864
	ds_read_b128 v[210:213], v130 offset:38912
	v_cvt_pk_f16_f32 v59, v58, v59
	v_cvt_pk_f16_f32 v58, v56, v57
	ds_write_b64 v100, v[58:59] offset:20480
	s_setprio 1
	s_waitcnt lgkmcnt(1)
	v_mfma_f32_16x16x32_f16 v[40:43], v[206:209], v[182:185], v[40:43]
	v_mfma_f32_16x16x32_f16 v[56:59], v[206:209], v[186:189], v[64:67]
	v_mfma_f32_16x16x32_f16 v[64:67], v[206:209], v[190:193], v[68:71]
	v_mfma_f32_16x16x32_f16 v[68:71], v[206:209], v[202:205], v[84:87]
	v_mfma_f32_16x16x32_f16 v[84:87], v[210:213], v[182:185], v[96:99]
	v_mfma_f32_16x16x32_f16 v[96:99], v[210:213], v[186:189], v[120:123]
	v_mfma_f32_16x16x32_f16 v[118:121], v[210:213], v[190:193], v[124:127]
	v_mfma_f32_16x16x32_f16 v[122:125], v[210:213], v[202:205], v[134:137]
	s_setprio 0
	s_nop 1
	ds_read_b128 v[134:137], v130 offset:40960
	ds_read_b128 v[206:209], v130 offset:43008
	v_cvt_pk_f16_f32 v63, v62, v63
	v_cvt_pk_f16_f32 v62, v60, v61
	ds_write_b64 v100, v[62:63] offset:24576
	s_setprio 1
	s_waitcnt lgkmcnt(1)
	v_mfma_f32_16x16x32_f16 v[44:47], v[134:137], v[182:185], v[44:47]
	v_mfma_f32_16x16x32_f16 v[60:63], v[134:137], v[186:189], v[72:75]
	v_mfma_f32_16x16x32_f16 v[72:75], v[134:137], v[190:193], v[88:91]
	v_mfma_f32_16x16x32_f16 v[88:91], v[134:137], v[202:205], v[138:141]
	v_mfma_f32_16x16x32_f16 v[134:137], v[206:209], v[182:185], v[146:149]
	v_mfma_f32_16x16x32_f16 v[146:149], v[206:209], v[190:193], v[162:165]
	v_mfma_f32_16x16x32_f16 v[138:141], v[206:209], v[186:189], v[150:153]
	v_mfma_f32_16x16x32_f16 v[142:145], v[206:209], v[202:205], v[142:145]
	s_setprio 0
	s_nop 0
	ds_read_b128 v[150:153], v130 offset:45056
	ds_read_b128 v[162:165], v130 offset:47104
	v_cvt_pk_f16_f32 v39, v38, v39
	v_cvt_pk_f16_f32 v38, v36, v37
	ds_write_b64 v100, v[38:39] offset:28672
	s_setprio 1
	s_waitcnt lgkmcnt(1)
	v_mfma_f32_16x16x32_f16 v[36:39], v[150:153], v[182:185], v[48:51]
	v_mfma_f32_16x16x32_f16 v[48:51], v[150:153], v[186:189], v[76:79]
	v_mfma_f32_16x16x32_f16 v[76:79], v[150:153], v[190:193], v[158:161]
	v_mfma_f32_16x16x32_f16 v[150:153], v[150:153], v[202:205], v[154:157]
	v_mfma_f32_16x16x32_f16 v[154:157], v[162:165], v[182:185], v[166:169]
	v_mfma_f32_16x16x32_f16 v[158:161], v[162:165], v[186:189], v[174:177]
	v_mfma_f32_16x16x32_f16 v[166:169], v[162:165], v[190:193], v[178:181]
	v_mfma_f32_16x16x32_f16 v[162:165], v[162:165], v[202:205], v[170:173]
	s_setprio 0
	s_waitcnt vmcnt(0)
	s_waitcnt lgkmcnt(0)
	s_barrier
	s_nop 0
	ds_read_b128 v[170:173], v131
	ds_read_b128 v[174:177], v131 offset:2048
	ds_read_b128 v[178:181], v131 offset:4096
	ds_read_b128 v[182:185], v131 offset:6144
	ds_read_b128 v[186:189], v129
	ds_read_b128 v[190:193], v129 offset:2048
	v_lshl_add_u64 v[126:127], s[56:57], 0, v[196:197]
	s_mov_b32 m0, s0
	v_cvt_pk_f16_f32 v3, v2, v3
	global_load_lds_dwordx4 v[126:127], off
	v_cvt_pk_f16_f32 v2, v0, v1
	ds_write_b64 v100, v[2:3] offset:32768
	s_setprio 1
	s_waitcnt lgkmcnt(1)
	v_mfma_f32_16x16x32_f16 v[0:3], v[186:189], v[170:173], v[8:11]
	v_mfma_f32_16x16x32_f16 v[8:11], v[186:189], v[174:177], v[52:55]
	v_mfma_f32_16x16x32_f16 v[52:55], v[186:189], v[178:181], v[80:83]
	v_mfma_f32_16x16x32_f16 v[80:83], v[186:189], v[182:185], v[92:95]
	v_mfma_f32_16x16x32_f16 v[92:95], v[190:193], v[170:173], v[102:105]
	v_mfma_f32_16x16x32_f16 v[102:105], v[190:193], v[174:177], v[106:109]
	v_mfma_f32_16x16x32_f16 v[106:109], v[190:193], v[178:181], v[110:113]
	v_mfma_f32_16x16x32_f16 v[110:113], v[190:193], v[182:185], v[114:117]
	s_setprio 0
	s_nop 1
	ds_read_b128 v[114:117], v129 offset:4096
	ds_read_b128 v[186:189], v129 offset:6144
	s_mov_b32 m0, s1
	v_lshl_add_u64 v[190:191], v[126:127], 0, s[58:59]
	global_load_lds_dwordx4 v[190:191], off
	v_cvt_pk_f16_f32 v7, v6, v7
	v_cvt_pk_f16_f32 v6, v4, v5
	ds_write_b64 v100, v[6:7] offset:36864
	s_setprio 1
	s_waitcnt lgkmcnt(1)
	v_mfma_f32_16x16x32_f16 v[190:193], v[114:117], v[170:173], v[40:43]
	v_mfma_f32_16x16x32_f16 v[56:59], v[114:117], v[174:177], v[56:59]
	v_mfma_f32_16x16x32_f16 v[64:67], v[114:117], v[178:181], v[64:67]
	v_mfma_f32_16x16x32_f16 v[68:71], v[114:117], v[182:185], v[68:71]
	v_mfma_f32_16x16x32_f16 v[84:87], v[186:189], v[170:173], v[84:87]
	v_mfma_f32_16x16x32_f16 v[96:99], v[186:189], v[174:177], v[96:99]
	v_mfma_f32_16x16x32_f16 v[114:117], v[186:189], v[178:181], v[118:121]
	v_mfma_f32_16x16x32_f16 v[118:121], v[186:189], v[182:185], v[122:125]
	s_setprio 0
	ds_read_b128 v[4:7], v129 offset:8192
	ds_read_b128 v[40:43], v129 offset:10240
	s_mov_b32 m0, s70
	v_lshl_add_u64 v[122:123], v[126:127], 0, s[60:61]
	global_load_lds_dwordx4 v[122:123], off
	v_cvt_pk_f16_f32 v15, v14, v15
	v_cvt_pk_f16_f32 v14, v12, v13
	ds_write_b64 v100, v[14:15] offset:40960
	s_setprio 1
	s_waitcnt lgkmcnt(1)
	v_mfma_f32_16x16x32_f16 v[122:125], v[4:7], v[170:173], v[44:47]
	v_mfma_f32_16x16x32_f16 v[88:91], v[4:7], v[182:185], v[88:91]
	v_mfma_f32_16x16x32_f16 v[134:137], v[40:43], v[170:173], v[134:137]
	v_mfma_f32_16x16x32_f16 v[146:149], v[40:43], v[178:181], v[146:149]
	v_mfma_f32_16x16x32_f16 v[186:189], v[4:7], v[174:177], v[60:63]
	v_mfma_f32_16x16x32_f16 v[202:205], v[4:7], v[178:181], v[72:75]
	v_mfma_f32_16x16x32_f16 v[138:141], v[40:43], v[174:177], v[138:141]
	v_mfma_f32_16x16x32_f16 v[142:145], v[40:43], v[182:185], v[142:145]
	s_setprio 0
	ds_read_b128 v[4:7], v129 offset:12288
	ds_read_b128 v[12:15], v129 offset:14336
	s_mov_b32 m0, s71
	v_lshl_add_u64 v[40:41], v[126:127], 0, s[62:63]
	global_load_lds_dwordx4 v[40:41], off
	v_cvt_pk_f16_f32 v19, v18, v19
	v_cvt_pk_f16_f32 v18, v16, v17
	ds_write_b64 v100, v[18:19] offset:45056
	s_setprio 1
	s_waitcnt lgkmcnt(1)
	v_mfma_f32_16x16x32_f16 v[206:209], v[4:7], v[170:173], v[36:39]
	v_mfma_f32_16x16x32_f16 v[210:213], v[4:7], v[174:177], v[48:51]
	v_mfma_f32_16x16x32_f16 v[214:217], v[4:7], v[178:181], v[76:79]
	v_mfma_f32_16x16x32_f16 v[150:153], v[4:7], v[182:185], v[150:153]
	v_mfma_f32_16x16x32_f16 v[154:157], v[12:15], v[170:173], v[154:157]
	v_mfma_f32_16x16x32_f16 v[158:161], v[12:15], v[174:177], v[158:161]
	v_mfma_f32_16x16x32_f16 v[166:169], v[12:15], v[178:181], v[166:169]
	v_mfma_f32_16x16x32_f16 v[162:165], v[12:15], v[182:185], v[162:165]
	s_setprio 0
	ds_read_b128 v[170:173], v128
	ds_read_b128 v[174:177], v128 offset:2048
	ds_read_b128 v[178:181], v128 offset:4096
	ds_read_b128 v[182:185], v128 offset:6144
	ds_read_b128 v[12:15], v130
	ds_read_b128 v[40:43], v130 offset:2048
	v_cvt_pk_f16_f32 v5, v22, v23
	v_cvt_pk_f16_f32 v4, v20, v21
	ds_write_b64 v100, v[4:5] offset:49152
	s_setprio 1
	s_waitcnt lgkmcnt(1)
	v_mfma_f32_16x16x32_f16 v[0:3], v[12:15], v[170:173], v[0:3]
	v_mfma_f32_16x16x32_f16 v[4:7], v[12:15], v[174:177], v[8:11]
	v_mfma_f32_16x16x32_f16 v[8:11], v[12:15], v[178:181], v[52:55]
	v_mfma_f32_16x16x32_f16 v[12:15], v[12:15], v[182:185], v[80:83]
	v_mfma_f32_16x16x32_f16 v[16:19], v[40:43], v[170:173], v[92:95]
	v_mfma_f32_16x16x32_f16 v[20:23], v[40:43], v[174:177], v[102:105]
	v_mfma_f32_16x16x32_f16 v[36:39], v[40:43], v[178:181], v[106:109]
	v_mfma_f32_16x16x32_f16 v[40:43], v[40:43], v[182:185], v[110:113]
	s_setprio 0
	ds_read_b128 v[52:55], v130 offset:4096
	ds_read_b128 v[72:75], v130 offset:6144
	v_cvt_pk_f16_f32 v27, v26, v27
	v_cvt_pk_f16_f32 v26, v24, v25
	ds_write_b64 v100, v[26:27] offset:53248
	s_setprio 1
	s_waitcnt lgkmcnt(1)
	v_mfma_f32_16x16x32_f16 v[24:27], v[52:55], v[170:173], v[190:193]
	v_mfma_f32_16x16x32_f16 v[44:47], v[52:55], v[174:177], v[56:59]
	v_mfma_f32_16x16x32_f16 v[48:51], v[52:55], v[178:181], v[64:67]
	v_mfma_f32_16x16x32_f16 v[52:55], v[52:55], v[182:185], v[68:71]
	v_mfma_f32_16x16x32_f16 v[56:59], v[72:75], v[170:173], v[84:87]
	v_mfma_f32_16x16x32_f16 v[60:63], v[72:75], v[174:177], v[96:99]
	v_mfma_f32_16x16x32_f16 v[64:67], v[72:75], v[178:181], v[114:117]
	v_mfma_f32_16x16x32_f16 v[68:71], v[72:75], v[182:185], v[118:121]
	s_setprio 0
	ds_read_b128 v[80:83], v130 offset:8192
	ds_read_b128 v[96:99], v130 offset:10240
	v_cvt_pk_f16_f32 v31, v30, v31
	v_cvt_pk_f16_f32 v30, v28, v29
	ds_write_b64 v100, v[30:31] offset:57344
	s_setprio 1
	s_waitcnt lgkmcnt(1)
	v_mfma_f32_16x16x32_f16 v[28:31], v[80:83], v[170:173], v[122:125]
	v_mfma_f32_16x16x32_f16 v[72:75], v[80:83], v[174:177], v[186:189]
	v_mfma_f32_16x16x32_f16 v[76:79], v[80:83], v[178:181], v[202:205]
	v_mfma_f32_16x16x32_f16 v[80:83], v[80:83], v[182:185], v[88:91]
	v_mfma_f32_16x16x32_f16 v[84:87], v[96:99], v[170:173], v[134:137]
	v_mfma_f32_16x16x32_f16 v[88:91], v[96:99], v[174:177], v[138:141]
	v_mfma_f32_16x16x32_f16 v[92:95], v[96:99], v[178:181], v[146:149]
	v_mfma_f32_16x16x32_f16 v[96:99], v[96:99], v[182:185], v[142:145]
	s_setprio 0
	ds_read_b128 v[108:111], v130 offset:12288
	ds_read_b128 v[124:127], v130 offset:14336
	v_cvt_pk_f16_f32 v35, v34, v35
	v_cvt_pk_f16_f32 v34, v32, v33
	ds_write_b64 v100, v[34:35] offset:61440
	s_setprio 1
	s_waitcnt lgkmcnt(1)
	v_mfma_f32_16x16x32_f16 v[32:35], v[108:111], v[170:173], v[206:209]
	v_mfma_f32_16x16x32_f16 v[100:103], v[108:111], v[174:177], v[210:213]
	v_mfma_f32_16x16x32_f16 v[104:107], v[108:111], v[178:181], v[214:217]
	v_mfma_f32_16x16x32_f16 v[108:111], v[108:111], v[182:185], v[150:153]
	v_mfma_f32_16x16x32_f16 v[112:115], v[124:127], v[170:173], v[154:157]
	v_mfma_f32_16x16x32_f16 v[116:119], v[124:127], v[174:177], v[158:161]
	v_mfma_f32_16x16x32_f16 v[120:123], v[124:127], v[178:181], v[166:169]
	v_mfma_f32_16x16x32_f16 v[124:127], v[124:127], v[182:185], v[162:165]
	s_setprio 0
	s_waitcnt vmcnt(0)
	s_waitcnt lgkmcnt(0)
	s_barrier
	ds_read_b128 v[134:137], v131 offset:32768
	ds_read_b128 v[138:141], v131 offset:34816
	ds_read_b128 v[142:145], v131 offset:36864
	ds_read_b128 v[148:151], v131 offset:38912
	ds_read_b128 v[152:155], v129 offset:32768
	ds_read_b128 v[156:159], v129 offset:34816
	s_setprio 1
	s_waitcnt lgkmcnt(0)
	v_mfma_f32_16x16x32_f16 v[0:3], v[152:155], v[134:137], v[0:3]
	v_mfma_f32_16x16x32_f16 v[4:7], v[152:155], v[138:141], v[4:7]
	v_mfma_f32_16x16x32_f16 v[8:11], v[152:155], v[142:145], v[8:11]
	v_mfma_f32_16x16x32_f16 v[12:15], v[152:155], v[148:151], v[12:15]
	v_mfma_f32_16x16x32_f16 v[16:19], v[156:159], v[134:137], v[16:19]
	v_mfma_f32_16x16x32_f16 v[20:23], v[156:159], v[138:141], v[20:23]
	v_mfma_f32_16x16x32_f16 v[36:39], v[156:159], v[142:145], v[36:39]
	v_mfma_f32_16x16x32_f16 v[40:43], v[156:159], v[148:151], v[40:43]
	s_setprio 0
	ds_read_b128 v[152:155], v129 offset:36864
	ds_read_b128 v[156:159], v129 offset:38912
	v_and_b32_e32 v250, 0x7ffffc00, v194
	v_lshl_add_u64 v[252:253], s[10:11], 0, v[196:197]
	v_readfirstlane_b32 s32, v250
	s_nop 0
	s_mov_b32 m0, s32
	s_nop 0
	global_load_lds_dwordx4 v[252:253], off
	v_mov_b32_e32 v146, 0
	v_and_b32_e32 v251, 0xfffffff, v132
	v_cmp_gt_u32_e32 vcc, s82, v251
	v_mov_b32_e32 v132, 0
	v_mov_b32_e32 v133, 0
	s_and_saveexec_b64 s[0:1], vcc
	s_cbranch_execz .LBB1_7
	s_and_b32 s64, s78, 0x7ffffc00
	s_or_b32 s64, s64, s33
	v_or_b32_e32 v132, s64, v251
	v_mov_b32_e32 v133, v195
	v_lshl_add_u64 v[132:133], v[132:133], 2, s[12:13]
	global_load_dword v133, v[132:133], off
	v_or_b32_e32 v132, s33, v251
	v_lshlrev_b32_e32 v132, 2, v132
	global_load_dword v146, v132, s[16:17]
	s_nop 0
	global_load_dword v132, v132, s[14:15]

	.amdhsa_kernel _Z11main_kernelPKDF16_PKfPKiS0_S2_S2_S2_PfS5_
		.amdhsa_group_segment_fixed_size 163840
		.amdhsa_private_segment_fixed_size 0
		.amdhsa_kernarg_size 72
		.amdhsa_user_sgpr_count 2
		.amdhsa_user_sgpr_dispatch_ptr 0
		.amdhsa_user_sgpr_queue_ptr 0
		.amdhsa_user_sgpr_kernarg_segment_ptr 1
		.amdhsa_user_sgpr_dispatch_id 0
		.amdhsa_user_sgpr_kernarg_preload_length 0
		.amdhsa_user_sgpr_kernarg_preload_offset 0
		.amdhsa_user_sgpr_private_segment_size 0
		.amdhsa_uses_dynamic_stack 0
		.amdhsa_enable_private_segment 0
		.amdhsa_system_sgpr_workgroup_id_x 1
		.amdhsa_system_sgpr_workgroup_id_y 0
		.amdhsa_system_sgpr_workgroup_id_z 0
		.amdhsa_system_sgpr_workgroup_info 0
		.amdhsa_system_vgpr_workitem_id 0
		.amdhsa_next_free_vgpr 256
		.amdhsa_next_free_sgpr 102
		.amdhsa_accum_offset 256
		.amdhsa_reserve_vcc 1
		.amdhsa_float_round_mode_32 0
		.amdhsa_float_round_mode_16_64 0
		.amdhsa_float_denorm_mode_32 3
		.amdhsa_float_denorm_mode_16_64 3
		.amdhsa_dx10_clamp 1
		.amdhsa_ieee_mode 1
		.amdhsa_fp16_overflow 0
		.amdhsa_tg_split 0
		.amdhsa_exception_fp_ieee_invalid_op 0
		.amdhsa_exception_fp_denorm_src 0
		.amdhsa_exception_fp_ieee_div_zero 0
		.amdhsa_exception_fp_ieee_overflow 0
		.amdhsa_exception_fp_ieee_underflow 0
		.amdhsa_exception_fp_ieee_inexact 0
		.amdhsa_exception_int_div_zero 0
	.end_amdhsa_kernel

amdhsa.kernels:
  - .agpr_count:     0
    .args:
      - .actual_access:  read_only
        .address_space:  global
        .offset:         0
        .size:           8
        .value_kind:     global_buffer
      - .actual_access:  read_only
        .address_space:  global
        .offset:         8
        .size:           8
        .value_kind:     global_buffer
      - .actual_access:  read_only
        .address_space:  global
        .offset:         16
        .size:           8
        .value_kind:     global_buffer
      - .actual_access:  read_only
        .address_space:  global
        .offset:         24
        .size:           8
        .value_kind:     global_buffer
      - .actual_access:  read_only
        .address_space:  global
        .offset:         32
        .size:           8
        .value_kind:     global_buffer
      - .actual_access:  write_only
        .address_space:  global
        .offset:         40
        .size:           8
        .value_kind:     global_buffer
      - .actual_access:  write_only
        .address_space:  global
        .offset:         48
        .size:           8
        .value_kind:     global_buffer
      - .actual_access:  write_only
        .address_space:  global
        .offset:         56
        .size:           8
        .value_kind:     global_buffer
    .group_segment_fixed_size: 0
    .kernarg_segment_align: 8
    .kernarg_segment_size: 64
    .language:       OpenCL C
    .language_version:
      - 2
      - 0
    .max_flat_workgroup_size: 256
    .name:           _Z11prep_kernelPKfS0_S0_S0_S0_PDF16_S1_Pf
    .private_segment_fixed_size: 0
    .sgpr_count:     30
    .sgpr_spill_count: 0
    .symbol:         _Z11prep_kernelPKfS0_S0_S0_S0_PDF16_S1_Pf.kd
    .uniform_work_group_size: 1
    .uses_dynamic_stack: false
    .vgpr_count:     236
    .vgpr_spill_count: 0
    .wavefront_size: 64
  - .agpr_count:     0
    .args:
      - .address_space:  global
        .offset:         0
        .size:           8
        .value_kind:     global_buffer
      - .address_space:  global
        .offset:         8
        .size:           8
        .value_kind:     global_buffer
      - .actual_access:  read_only
        .address_space:  global
        .offset:         16
        .size:           8
        .value_kind:     global_buffer
      - .address_space:  global
        .offset:         24
        .size:           8
        .value_kind:     global_buffer
      - .actual_access:  read_only
        .address_space:  global
        .offset:         32
        .size:           8
        .value_kind:     global_buffer
      - .actual_access:  read_only
        .address_space:  global
        .offset:         40
        .size:           8
        .value_kind:     global_buffer
      - .actual_access:  read_only
        .address_space:  global
        .offset:         48
        .size:           8
        .value_kind:     global_buffer
      - .actual_access:  write_only
        .address_space:  global
        .offset:         56
        .size:           8
        .value_kind:     global_buffer
      - .actual_access:  write_only
        .address_space:  global
        .offset:         64
        .size:           8
        .value_kind:     global_buffer
    .group_segment_fixed_size: 163840
    .kernarg_segment_align: 8
    .kernarg_segment_size: 72
    .language:       OpenCL C
    .language_version:
      - 2
      - 0
    .max_flat_workgroup_size: 512
    .name:           _Z11main_kernelPKDF16_PKfPKiS0_S2_S2_S2_PfS5_
    .private_segment_fixed_size: 0
    .sgpr_count:     108
    .sgpr_spill_count: 0
    .symbol:         _Z11main_kernelPKDF16_PKfPKiS0_S2_S2_S2_PfS5_.kd
    .uniform_work_group_size: 1
    .uses_dynamic_stack: false
    .vgpr_count:     256
    .vgpr_spill_count: 0
    .wavefront_size: 64
  - .agpr_count:     0
    .args:
      - .actual_access:  read_only
        .address_space:  global
        .offset:         0
        .size:           8
        .value_kind:     global_buffer
      - .actual_access:  read_only
        .address_space:  global
        .offset:         8
        .size:           8
        .value_kind:     global_buffer
      - .actual_access:  write_only
        .address_space:  global
        .offset:         16
        .size:           8
        .value_kind:     global_buffer
    .group_segment_fixed_size: 32
    .kernarg_segment_align: 8
    .kernarg_segment_size: 24
    .language:       OpenCL C
    .language_version:
      - 2
      - 0
    .max_flat_workgroup_size: 256
    .name:           _Z14combine_kernelPKfS0_Pf
    .private_segment_fixed_size: 0
    .sgpr_count:     26
    .sgpr_spill_count: 0
    .symbol:         _Z14combine_kernelPKfS0_Pf.kd
    .uniform_work_group_size: 1
    .uses_dynamic_stack: false
    .vgpr_count:     40
    .vgpr_spill_count: 0
    .wavefront_size: 64
